# nt (streaming) hint on the read-once loads: P7 projection values, phase-0 f32 weight reads
# speedup vs baseline: 1.0059x; 1.0059x over previous
.LBB0_78:
	v_or_b32_e32 v2, s4, v16
	s_or_b32 s5, s4, 2
	s_or_b32 s9, s4, 4
	s_or_b32 s16, s4, 6
	s_or_b32 s17, s4, 8
	s_or_b32 s41, s4, 10
	s_or_b32 s56, s4, 12
	s_or_b32 s59, s4, 14
	s_or_b32 s62, s4, 16
	s_or_b32 s63, s4, 18
	s_or_b32 s68, s4, 20
	s_or_b32 s69, s4, 22
	s_or_b32 s76, s4, 24
	s_or_b32 s77, s4, 26
	s_or_b32 s78, s4, 28
	s_or_b32 s79, s4, 30
	v_mul_hi_u32_u24_e32 v31, s40, v2
	v_mul_u32_u24_e32 v30, s40, v2
	v_lshl_add_u64 v[32:33], v[2:3], 2, s[74:75]
	v_or_b32_e32 v17, s5, v16
	v_or_b32_e32 v29, s9, v16
	v_or_b32_e32 v38, s16, v16
	v_or_b32_e32 v40, s17, v16
	v_or_b32_e32 v42, s41, v16
	v_or_b32_e32 v44, s56, v16
	v_or_b32_e32 v46, s59, v16
	v_add_u32_e32 v2, s4, v16
	v_or_b32_e32 v48, s62, v16
	v_or_b32_e32 v52, s63, v16
	v_or_b32_e32 v54, s68, v16
	v_or_b32_e32 v56, s69, v16
	v_or_b32_e32 v58, s76, v16
	v_or_b32_e32 v60, s77, v16
	v_or_b32_e32 v62, s78, v16
	v_or_b32_e32 v64, s79, v16
	v_lshl_add_u64 v[30:31], v[30:31], 2, v[14:15]
	global_load_dword v66, v[32:33], off nt
	v_mul_hi_u32_u24_e32 v33, s40, v17
	v_mul_u32_u24_e32 v32, s40, v17
	v_mul_hi_u32_u24_e32 v37, s40, v29
	v_mul_u32_u24_e32 v36, s40, v29
	v_mul_hi_u32_u24_e32 v39, s40, v38
	v_mul_u32_u24_e32 v38, s40, v38
	v_mul_hi_u32_u24_e32 v41, s40, v40
	v_mul_u32_u24_e32 v40, s40, v40
	v_mul_hi_u32_u24_e32 v43, s40, v42
	v_mul_u32_u24_e32 v42, s40, v42
	v_mul_hi_u32_u24_e32 v45, s40, v44
	v_mul_u32_u24_e32 v44, s40, v44
	v_mul_hi_u32_u24_e32 v47, s40, v46
	v_mul_u32_u24_e32 v46, s40, v46
	v_lshl_add_u64 v[34:35], v[2:3], 2, s[74:75]
	v_mul_hi_u32_u24_e32 v49, s40, v48
	v_mul_u32_u24_e32 v48, s40, v48
	v_mul_hi_u32_u24_e32 v53, s40, v52
	v_mul_u32_u24_e32 v52, s40, v52
	v_mul_hi_u32_u24_e32 v55, s40, v54
	v_mul_u32_u24_e32 v54, s40, v54
	v_mul_hi_u32_u24_e32 v57, s40, v56
	v_mul_u32_u24_e32 v56, s40, v56
	v_mul_hi_u32_u24_e32 v59, s40, v58
	v_mul_u32_u24_e32 v58, s40, v58
	v_mul_hi_u32_u24_e32 v61, s40, v60
	v_mul_u32_u24_e32 v60, s40, v60
	v_mul_hi_u32_u24_e32 v63, s40, v62
	v_mul_u32_u24_e32 v62, s40, v62
	v_mul_hi_u32_u24_e32 v65, s40, v64
	v_mul_u32_u24_e32 v64, s40, v64
	global_load_dword v2, v[30:31], off nt
	v_lshl_add_u64 v[30:31], v[32:33], 2, v[14:15]
	v_lshl_add_u64 v[32:33], v[36:37], 2, v[14:15]
	v_lshl_add_u64 v[36:37], v[38:39], 2, v[14:15]
	v_lshl_add_u64 v[38:39], v[40:41], 2, v[14:15]
	v_lshl_add_u64 v[40:41], v[42:43], 2, v[14:15]
	v_lshl_add_u64 v[42:43], v[44:45], 2, v[14:15]
	v_lshl_add_u64 v[44:45], v[46:47], 2, v[14:15]
	v_lshl_add_u64 v[46:47], v[48:49], 2, v[14:15]
	global_load_dword v17, v[34:35], off offset:8 nt
	global_load_dword v29, v[34:35], off offset:16 nt
	global_load_dword v67, v[34:35], off offset:24 nt
	global_load_dword v68, v[34:35], off offset:32 nt
	global_load_dword v69, v[34:35], off offset:40 nt
	global_load_dword v70, v[34:35], off offset:48 nt
	global_load_dword v71, v[34:35], off offset:56 nt
	global_load_dword v72, v[34:35], off offset:64 nt
	v_lshl_add_u64 v[48:49], v[52:53], 2, v[14:15]
	v_lshl_add_u64 v[52:53], v[54:55], 2, v[14:15]
	v_lshl_add_u64 v[54:55], v[56:57], 2, v[14:15]
	v_lshl_add_u64 v[56:57], v[58:59], 2, v[14:15]
	v_lshl_add_u64 v[58:59], v[60:61], 2, v[14:15]
	v_lshl_add_u64 v[60:61], v[62:63], 2, v[14:15]
	v_lshl_add_u64 v[62:63], v[64:65], 2, v[14:15]
	global_load_dword v64, v[34:35], off offset:72 nt
	global_load_dword v65, v[34:35], off offset:80 nt
	global_load_dword v73, v[34:35], off offset:88 nt
	global_load_dword v74, v[34:35], off offset:96 nt
	global_load_dword v75, v[34:35], off offset:104 nt
	global_load_dword v76, v[34:35], off offset:112 nt
	s_nop 0
	global_load_dword v34, v[34:35], off offset:120 nt
	s_nop 0
	global_load_dword v30, v[30:31], off nt
	s_nop 0
	global_load_dword v31, v[32:33], off nt
	s_nop 0
	global_load_dword v32, v[36:37], off nt
	global_load_dword v33, v[38:39], off nt
	global_load_dword v35, v[40:41], off nt
	s_nop 0
	global_load_dword v36, v[42:43], off nt
	global_load_dword v37, v[44:45], off nt
	global_load_dword v38, v[46:47], off nt
	global_load_dword v39, v[48:49], off nt
	global_load_dword v40, v[52:53], off nt
	global_load_dword v41, v[54:55], off nt
	global_load_dword v42, v[56:57], off nt
	global_load_dword v43, v[58:59], off nt
	global_load_dword v44, v[60:61], off nt
	global_load_dword v45, v[62:63], off nt
	v_or_b32_e32 v46, s4, v18
	s_and_b64 vcc, exec, s[36:37]
	s_mov_b64 s[36:37], 0
	v_mad_u32_u24 v46, v46, s66, v19
	v_or_b32_e32 v47, s5, v18
	v_or_b32_e32 v48, s9, v18
	v_or_b32_e32 v49, s16, v18
	v_or_b32_e32 v52, s17, v18
	v_or_b32_e32 v53, s41, v18
	v_or_b32_e32 v54, s56, v18
	v_or_b32_e32 v55, s59, v18
	v_or_b32_e32 v56, s62, v18
	v_or_b32_e32 v57, s63, v18
	v_or_b32_e32 v58, s68, v18
	v_or_b32_e32 v59, s69, v18
	v_or_b32_e32 v60, s76, v18
	v_or_b32_e32 v61, s77, v18
	v_or_b32_e32 v62, s78, v18
	v_or_b32_e32 v63, s79, v18
	s_mov_b32 s4, 32
	v_mad_u32_u24 v47, v47, s66, v19
	v_mad_u32_u24 v48, v48, s66, v19
	v_mad_u32_u24 v49, v49, s66, v19
	v_mad_u32_u24 v52, v52, s66, v19
	v_mad_u32_u24 v53, v53, s66, v19
	v_mad_u32_u24 v54, v54, s66, v19
	v_mad_u32_u24 v55, v55, s66, v19
	v_mad_u32_u24 v56, v56, s66, v19
	v_mad_u32_u24 v57, v57, s66, v19
	v_mad_u32_u24 v58, v58, s66, v19
	v_mad_u32_u24 v59, v59, s66, v19
	v_mad_u32_u24 v60, v60, s66, v19
	v_mad_u32_u24 v61, v61, s66, v19
	v_mad_u32_u24 v62, v62, s66, v19
	v_mad_u32_u24 v63, v63, s66, v19
	s_waitcnt vmcnt(0)
	v_mul_f32_e32 v2, v2, v66
	s_waitcnt vmcnt(14)
	v_mul_f32_e32 v17, v30, v17
	s_waitcnt vmcnt(13)
	v_mul_f32_e32 v29, v31, v29
	s_waitcnt vmcnt(12)
	v_mul_f32_e32 v30, v32, v67
	s_waitcnt vmcnt(11)
	v_mul_f32_e32 v31, v33, v68
	s_waitcnt vmcnt(10)
	v_mul_f32_e32 v32, v35, v69
	s_waitcnt vmcnt(9)
	v_mul_f32_e32 v33, v36, v70
	s_waitcnt vmcnt(8)
	v_mul_f32_e32 v35, v37, v71
	s_waitcnt vmcnt(7)
	v_mul_f32_e32 v36, v38, v72
	s_waitcnt vmcnt(6)
	v_mul_f32_e32 v37, v39, v64
	s_waitcnt vmcnt(5)
	v_mul_f32_e32 v38, v40, v65
	s_waitcnt vmcnt(4)
	v_mul_f32_e32 v39, v41, v73
	s_waitcnt vmcnt(3)
	v_mul_f32_e32 v40, v42, v74
	s_waitcnt vmcnt(2)
	v_mul_f32_e32 v41, v43, v75
	s_waitcnt vmcnt(1)
	v_mul_f32_e32 v42, v44, v76
	s_waitcnt vmcnt(0)
	v_mul_f32_e32 v34, v45, v34
	ds_write_b32 v46, v2
	ds_write_b32 v47, v17
	ds_write_b32 v48, v29
	ds_write_b32 v49, v30
	ds_write_b32 v52, v31
	ds_write_b32 v53, v32
	ds_write_b32 v54, v33
	ds_write_b32 v55, v35
	ds_write_b32 v56, v36
	ds_write_b32 v57, v37
	ds_write_b32 v58, v38
	ds_write_b32 v59, v39
	ds_write_b32 v60, v40
	ds_write_b32 v61, v41
	ds_write_b32 v62, v42
	ds_write_b32 v63, v34
	s_cbranch_vccnz .LBB0_78
	s_waitcnt lgkmcnt(0)
	ds_read2_b32 v[34:35], v21 offset1:8
	ds_read2_b32 v[38:39], v21 offset0:33 offset1:41
	s_lshl_b32 s4, s7, 1
	s_add_u32 s4, s38, s4
	ds_read2_b32 v[40:41], v21 offset0:66 offset1:74
	s_addc_u32 s5, s39, 0
	v_lshlrev_b32_e32 v2, 1, v4
	ds_read2_b32 v[42:43], v21 offset0:99 offset1:107
	v_lshl_add_u64 v[36:37], s[4:5], 0, v[2:3]
	s_waitcnt lgkmcnt(3)
	v_bfe_u32 v2, v34, 16, 1
	v_add3_u32 v2, v34, v2, s1
	s_waitcnt lgkmcnt(2)
	v_bfe_u32 v17, v38, 16, 1
	ds_read2_b32 v[44:45], v21 offset0:132 offset1:140
	v_lshrrev_b32_e32 v2, 16, v2
	v_add3_u32 v17, v38, v17, s1
	ds_read2_b32 v[46:47], v21 offset0:165 offset1:173
	v_and_or_b32 v30, v17, s0, v2
	s_waitcnt lgkmcnt(3)
	v_bfe_u32 v2, v40, 16, 1
	v_add3_u32 v2, v40, v2, s1
	s_waitcnt lgkmcnt(2)
	v_bfe_u32 v17, v42, 16, 1
	ds_read2_b32 v[48:49], v21 offset0:198 offset1:206
	v_lshrrev_b32_e32 v2, 16, v2
	v_add3_u32 v17, v42, v17, s1
	ds_read2_b32 v[52:53], v21 offset0:231 offset1:239
	v_and_or_b32 v31, v17, s0, v2
	s_waitcnt lgkmcnt(3)
	v_bfe_u32 v2, v44, 16, 1
	v_add3_u32 v2, v44, v2, s1
	s_waitcnt lgkmcnt(2)
	v_bfe_u32 v17, v46, 16, 1
	v_lshrrev_b32_e32 v2, 16, v2
	v_add3_u32 v17, v46, v17, s1
	v_and_or_b32 v32, v17, s0, v2
	s_waitcnt lgkmcnt(1)
	v_bfe_u32 v2, v48, 16, 1
	v_add3_u32 v2, v48, v2, s1
	s_waitcnt lgkmcnt(0)
	v_bfe_u32 v17, v52, 16, 1
	v_lshrrev_b32_e32 v2, 16, v2
	v_add3_u32 v17, v52, v17, s1
	v_and_or_b32 v33, v17, s0, v2
	v_or_b32_e32 v2, s6, v20
	v_mul_hi_u32_u24_e32 v55, s8, v2
	v_mul_u32_u24_e32 v54, s8, v2
	v_bfe_u32 v2, v35, 16, 1
	v_add3_u32 v2, v35, v2, s1
	v_bfe_u32 v17, v39, 16, 1
	v_lshl_add_u64 v[54:55], v[54:55], 1, v[36:37]
	v_lshrrev_b32_e32 v2, 16, v2
	v_add3_u32 v17, v39, v17, s1
	global_store_dwordx4 v[54:55], v[30:33], off
	ds_read2_b32 v[38:39], v21 offset0:16 offset1:24
	s_nop 0
	v_and_or_b32 v30, v17, s0, v2
	v_bfe_u32 v2, v41, 16, 1
	v_add3_u32 v2, v41, v2, s1
	v_bfe_u32 v17, v43, 16, 1
	v_lshrrev_b32_e32 v2, 16, v2
	v_add3_u32 v17, v43, v17, s1
	v_and_or_b32 v31, v17, s0, v2
	v_bfe_u32 v2, v45, 16, 1
	v_add3_u32 v2, v45, v2, s1
	v_bfe_u32 v17, v47, 16, 1
	v_lshrrev_b32_e32 v2, 16, v2
	v_add3_u32 v17, v47, v17, s1
	v_and_or_b32 v32, v17, s0, v2
	v_bfe_u32 v2, v49, 16, 1
	v_add3_u32 v2, v49, v2, s1
	v_bfe_u32 v17, v53, 16, 1
	v_lshrrev_b32_e32 v2, 16, v2
	v_add3_u32 v17, v53, v17, s1
	v_and_or_b32 v33, v17, s0, v2
	v_or_b32_e32 v2, s6, v22
	v_mul_hi_u32_u24_e32 v35, s8, v2
	v_mul_u32_u24_e32 v34, s8, v2
	v_lshl_add_u64 v[34:35], v[34:35], 1, v[36:37]
	global_store_dwordx4 v[34:35], v[30:33], off
	ds_read2_b32 v[34:35], v21 offset0:49 offset1:57
	ds_read2_b32 v[40:41], v21 offset0:82 offset1:90
	ds_read2_b32 v[42:43], v21 offset0:115 offset1:123
	s_waitcnt lgkmcnt(3)
	v_bfe_u32 v2, v38, 16, 1
	v_add3_u32 v2, v38, v2, s1
	s_waitcnt lgkmcnt(2)
	v_bfe_u32 v17, v34, 16, 1
	ds_read2_b32 v[44:45], v21 offset0:148 offset1:156
	v_lshrrev_b32_e32 v2, 16, v2
	v_add3_u32 v17, v34, v17, s1
	ds_read2_b32 v[46:47], v21 offset0:181 offset1:189
	v_and_or_b32 v30, v17, s0, v2
	s_waitcnt lgkmcnt(3)
	v_bfe_u32 v2, v40, 16, 1
	v_add3_u32 v2, v40, v2, s1
	s_waitcnt lgkmcnt(2)
	v_bfe_u32 v17, v42, 16, 1
	ds_read2_b32 v[48:49], v21 offset0:214 offset1:222
	v_lshrrev_b32_e32 v2, 16, v2
	v_add3_u32 v17, v42, v17, s1
	ds_read2_b32 v[52:53], v21 offset0:247 offset1:255
	v_and_or_b32 v31, v17, s0, v2
	s_waitcnt lgkmcnt(3)
	v_bfe_u32 v2, v44, 16, 1
	v_add3_u32 v2, v44, v2, s1
	s_waitcnt lgkmcnt(2)
	v_bfe_u32 v17, v46, 16, 1
	v_lshrrev_b32_e32 v2, 16, v2
	v_add3_u32 v17, v46, v17, s1
	v_and_or_b32 v32, v17, s0, v2
	s_waitcnt lgkmcnt(1)
	v_bfe_u32 v2, v48, 16, 1
	v_add3_u32 v2, v48, v2, s1
	s_waitcnt lgkmcnt(0)
	v_bfe_u32 v17, v52, 16, 1
	v_lshrrev_b32_e32 v2, 16, v2
	v_add3_u32 v17, v52, v17, s1
	v_and_or_b32 v33, v17, s0, v2
	v_or_b32_e32 v2, s6, v23
	v_mul_hi_u32_u24_e32 v55, s8, v2
	v_mul_u32_u24_e32 v54, s8, v2
	v_bfe_u32 v2, v39, 16, 1
	v_add3_u32 v2, v39, v2, s1
	v_bfe_u32 v17, v35, 16, 1
	v_lshl_add_u64 v[54:55], v[54:55], 1, v[36:37]
	v_lshrrev_b32_e32 v2, 16, v2
	v_add3_u32 v17, v35, v17, s1
	global_store_dwordx4 v[54:55], v[30:33], off
	s_mov_b32 s79, 0x16000
	s_mov_b32 s62, 0x18000
	v_and_or_b32 v30, v17, s0, v2
	v_bfe_u32 v2, v41, 16, 1
	v_add3_u32 v2, v41, v2, s1
	v_bfe_u32 v17, v43, 16, 1
	v_lshrrev_b32_e32 v2, 16, v2
	v_add3_u32 v17, v43, v17, s1
	v_and_or_b32 v31, v17, s0, v2
	v_bfe_u32 v2, v45, 16, 1
	v_add3_u32 v2, v45, v2, s1
	v_bfe_u32 v17, v47, 16, 1
	v_lshrrev_b32_e32 v2, 16, v2
	v_add3_u32 v17, v47, v17, s1
	v_and_or_b32 v32, v17, s0, v2
	v_bfe_u32 v2, v49, 16, 1
	v_add3_u32 v2, v49, v2, s1
	v_bfe_u32 v17, v53, 16, 1
	v_lshrrev_b32_e32 v2, 16, v2
	v_add3_u32 v17, v53, v17, s1
	v_and_or_b32 v33, v17, s0, v2
	v_or_b32_e32 v2, s6, v24
	v_mul_hi_u32_u24_e32 v35, s8, v2
	v_mul_u32_u24_e32 v34, s8, v2
	v_lshl_add_u64 v[34:35], v[34:35], 1, v[36:37]
	global_store_dwordx4 v[34:35], v[30:33], off
	s_waitcnt lgkmcnt(0)
	s_mov_b32 s63, 0x1a000
	s_mov_b32 s78, 0xa000
	s_mov_b32 s77, 0xc000
	s_mov_b32 s76, 0xe000
	s_branch .LBB0_84

.LBB0_82:
	v_or_b32_e32 v2, s4, v16
	s_or_b32 s5, s4, 2
	s_or_b32 s9, s4, 4
	s_or_b32 s16, s4, 6
	s_or_b32 s17, s4, 8
	s_or_b32 s41, s4, 10
	s_or_b32 s56, s4, 12
	s_or_b32 s59, s4, 14
	s_or_b32 s62, s4, 16
	s_or_b32 s63, s4, 18
	s_or_b32 s68, s4, 20
	s_or_b32 s69, s4, 22
	s_or_b32 s74, s4, 24
	s_or_b32 s75, s4, 26
	s_or_b32 s76, s4, 28
	s_or_b32 s77, s4, 30
	v_mul_hi_u32_u24_e32 v31, s40, v2
	v_mul_u32_u24_e32 v30, s40, v2
	v_or_b32_e32 v2, s5, v16
	v_or_b32_e32 v17, s9, v16
	v_or_b32_e32 v29, s16, v16
	v_or_b32_e32 v38, s17, v16
	v_or_b32_e32 v40, s41, v16
	v_or_b32_e32 v42, s56, v16
	v_or_b32_e32 v44, s59, v16
	v_or_b32_e32 v46, s62, v16
	v_or_b32_e32 v48, s63, v16
	v_or_b32_e32 v52, s68, v16
	v_or_b32_e32 v54, s69, v16
	v_or_b32_e32 v56, s74, v16
	v_or_b32_e32 v58, s75, v16
	v_or_b32_e32 v60, s76, v16
	v_or_b32_e32 v62, s77, v16
	v_mul_hi_u32_u24_e32 v33, s40, v2
	v_mul_u32_u24_e32 v32, s40, v2
	v_mul_hi_u32_u24_e32 v35, s40, v17
	v_mul_u32_u24_e32 v34, s40, v17
	v_mul_hi_u32_u24_e32 v37, s40, v29
	v_mul_u32_u24_e32 v36, s40, v29
	v_mul_hi_u32_u24_e32 v39, s40, v38
	v_mul_u32_u24_e32 v38, s40, v38
	v_mul_hi_u32_u24_e32 v41, s40, v40
	v_mul_u32_u24_e32 v40, s40, v40
	v_mul_hi_u32_u24_e32 v43, s40, v42
	v_mul_u32_u24_e32 v42, s40, v42
	v_lshl_add_u64 v[30:31], v[30:31], 2, v[14:15]
	v_mul_hi_u32_u24_e32 v45, s40, v44
	v_mul_u32_u24_e32 v44, s40, v44
	v_mul_hi_u32_u24_e32 v47, s40, v46
	v_mul_u32_u24_e32 v46, s40, v46
	v_mul_hi_u32_u24_e32 v49, s40, v48
	v_mul_u32_u24_e32 v48, s40, v48
	v_mul_hi_u32_u24_e32 v53, s40, v52
	v_mul_u32_u24_e32 v52, s40, v52
	v_mul_hi_u32_u24_e32 v55, s40, v54
	v_mul_u32_u24_e32 v54, s40, v54
	v_mul_hi_u32_u24_e32 v57, s40, v56
	v_mul_u32_u24_e32 v56, s40, v56
	v_mul_hi_u32_u24_e32 v59, s40, v58
	v_mul_u32_u24_e32 v58, s40, v58
	v_mul_hi_u32_u24_e32 v61, s40, v60
	v_mul_u32_u24_e32 v60, s40, v60
	v_mul_hi_u32_u24_e32 v63, s40, v62
	v_mul_u32_u24_e32 v62, s40, v62
	v_lshl_add_u64 v[32:33], v[32:33], 2, v[14:15]
	v_lshl_add_u64 v[34:35], v[34:35], 2, v[14:15]
	v_lshl_add_u64 v[36:37], v[36:37], 2, v[14:15]
	v_lshl_add_u64 v[38:39], v[38:39], 2, v[14:15]
	v_lshl_add_u64 v[40:41], v[40:41], 2, v[14:15]
	v_lshl_add_u64 v[42:43], v[42:43], 2, v[14:15]
	v_lshl_add_u64 v[44:45], v[44:45], 2, v[14:15]
	v_lshl_add_u64 v[46:47], v[46:47], 2, v[14:15]
	v_lshl_add_u64 v[48:49], v[48:49], 2, v[14:15]
	v_lshl_add_u64 v[52:53], v[52:53], 2, v[14:15]
	v_lshl_add_u64 v[54:55], v[54:55], 2, v[14:15]
	v_lshl_add_u64 v[56:57], v[56:57], 2, v[14:15]
	v_lshl_add_u64 v[58:59], v[58:59], 2, v[14:15]
	v_lshl_add_u64 v[60:61], v[60:61], 2, v[14:15]
	v_lshl_add_u64 v[62:63], v[62:63], 2, v[14:15]
	global_load_dword v2, v[30:31], off nt
	global_load_dword v17, v[32:33], off nt
	global_load_dword v29, v[34:35], off nt
	s_nop 0
	global_load_dword v30, v[36:37], off nt
	global_load_dword v31, v[38:39], off nt
	global_load_dword v32, v[40:41], off nt
	global_load_dword v33, v[42:43], off nt
	global_load_dword v34, v[44:45], off nt
	global_load_dword v35, v[46:47], off nt
	global_load_dword v36, v[48:49], off nt
	global_load_dword v37, v[52:53], off nt
	global_load_dword v38, v[54:55], off nt
	global_load_dword v39, v[56:57], off nt
	global_load_dword v40, v[58:59], off nt
	global_load_dword v41, v[60:61], off nt
	global_load_dword v42, v[62:63], off nt
	v_or_b32_e32 v43, s4, v18
	s_mov_b32 s4, 32
	s_and_b64 vcc, exec, s[36:37]
	s_mov_b64 s[36:37], 0
	v_mad_u32_u24 v43, v43, s66, v19
	v_or_b32_e32 v44, s5, v18
	v_or_b32_e32 v45, s9, v18
	v_or_b32_e32 v46, s16, v18
	v_or_b32_e32 v47, s17, v18
	v_or_b32_e32 v48, s41, v18
	v_or_b32_e32 v49, s56, v18
	v_or_b32_e32 v52, s59, v18
	v_or_b32_e32 v53, s62, v18
	v_or_b32_e32 v54, s63, v18
	v_or_b32_e32 v55, s68, v18
	v_or_b32_e32 v56, s69, v18
	v_or_b32_e32 v57, s74, v18
	v_or_b32_e32 v58, s75, v18
	v_or_b32_e32 v59, s76, v18
	v_or_b32_e32 v60, s77, v18
	v_mad_u32_u24 v44, v44, s66, v19
	v_mad_u32_u24 v45, v45, s66, v19
	v_mad_u32_u24 v46, v46, s66, v19
	v_mad_u32_u24 v47, v47, s66, v19
	v_mad_u32_u24 v48, v48, s66, v19
	v_mad_u32_u24 v49, v49, s66, v19
	v_mad_u32_u24 v52, v52, s66, v19
	v_mad_u32_u24 v53, v53, s66, v19
	v_mad_u32_u24 v54, v54, s66, v19
	v_mad_u32_u24 v55, v55, s66, v19
	v_mad_u32_u24 v56, v56, s66, v19
	v_mad_u32_u24 v57, v57, s66, v19
	v_mad_u32_u24 v58, v58, s66, v19
	v_mad_u32_u24 v59, v59, s66, v19
	v_mad_u32_u24 v60, v60, s66, v19
	s_waitcnt vmcnt(0)
	ds_write_b32 v43, v2
	s_waitcnt vmcnt(14)
	ds_write_b32 v44, v17
	s_waitcnt vmcnt(13)
	ds_write_b32 v45, v29
	s_waitcnt vmcnt(12)
	ds_write_b32 v46, v30
	s_waitcnt vmcnt(11)
	ds_write_b32 v47, v31
	s_waitcnt vmcnt(10)
	ds_write_b32 v48, v32
	s_waitcnt vmcnt(9)
	ds_write_b32 v49, v33
	s_waitcnt vmcnt(8)
	ds_write_b32 v52, v34
	s_waitcnt vmcnt(7)
	ds_write_b32 v53, v35
	s_waitcnt vmcnt(6)
	ds_write_b32 v54, v36
	s_waitcnt vmcnt(5)
	ds_write_b32 v55, v37
	s_waitcnt vmcnt(4)
	ds_write_b32 v56, v38
	s_waitcnt vmcnt(3)
	ds_write_b32 v57, v39
	s_waitcnt vmcnt(2)
	ds_write_b32 v58, v40
	s_waitcnt vmcnt(1)
	ds_write_b32 v59, v41
	s_waitcnt vmcnt(0)
	ds_write_b32 v60, v42
	s_cbranch_vccnz .LBB0_82
	s_waitcnt lgkmcnt(0)
	ds_read2_b32 v[30:31], v21 offset1:8
	ds_read2_b32 v[34:35], v21 offset0:33 offset1:41
	s_lshl_b32 s4, s7, 1
	s_add_u32 s4, s38, s4
	ds_read2_b32 v[36:37], v21 offset0:66 offset1:74
	s_addc_u32 s5, s39, 0
	v_lshlrev_b32_e32 v2, 1, v4
	ds_read2_b32 v[38:39], v21 offset0:99 offset1:107
	v_lshl_add_u64 v[32:33], s[4:5], 0, v[2:3]
	s_waitcnt lgkmcnt(3)
	v_bfe_u32 v2, v30, 16, 1
	v_add3_u32 v2, v30, v2, s1
	s_waitcnt lgkmcnt(2)
	v_bfe_u32 v14, v34, 16, 1
	ds_read2_b32 v[40:41], v21 offset0:132 offset1:140
	v_lshrrev_b32_e32 v2, 16, v2
	v_add3_u32 v14, v34, v14, s1
	ds_read2_b32 v[42:43], v21 offset0:165 offset1:173
	v_and_or_b32 v14, v14, s0, v2
	s_waitcnt lgkmcnt(3)
	v_bfe_u32 v2, v36, 16, 1
	v_add3_u32 v2, v36, v2, s1
	s_waitcnt lgkmcnt(2)
	v_bfe_u32 v15, v38, 16, 1
	ds_read2_b32 v[44:45], v21 offset0:198 offset1:206
	v_lshrrev_b32_e32 v2, 16, v2
	v_add3_u32 v15, v38, v15, s1
	ds_read2_b32 v[46:47], v21 offset0:231 offset1:239
	v_and_or_b32 v15, v15, s0, v2
	s_waitcnt lgkmcnt(3)
	v_bfe_u32 v2, v40, 16, 1
	v_add3_u32 v2, v40, v2, s1
	s_waitcnt lgkmcnt(2)
	v_bfe_u32 v16, v42, 16, 1
	v_lshrrev_b32_e32 v2, 16, v2
	v_add3_u32 v16, v42, v16, s1
	v_and_or_b32 v16, v16, s0, v2
	s_waitcnt lgkmcnt(1)
	v_bfe_u32 v2, v44, 16, 1
	v_add3_u32 v2, v44, v2, s1
	s_waitcnt lgkmcnt(0)
	v_bfe_u32 v17, v46, 16, 1
	v_lshrrev_b32_e32 v2, 16, v2
	v_add3_u32 v17, v46, v17, s1
	v_and_or_b32 v17, v17, s0, v2
	v_or_b32_e32 v2, s6, v20
	v_mul_hi_u32_u24_e32 v49, s8, v2
	v_mul_u32_u24_e32 v48, s8, v2
	v_lshl_add_u64 v[48:49], v[48:49], 1, v[32:33]
	v_bfe_u32 v2, v31, 16, 1
	global_store_dwordx4 v[48:49], v[14:17], off
	v_add3_u32 v2, v31, v2, s1
	v_lshrrev_b32_e32 v2, 16, v2
	v_bfe_u32 v14, v35, 16, 1
	v_add3_u32 v14, v35, v14, s1
	v_and_or_b32 v14, v14, s0, v2
	v_bfe_u32 v2, v37, 16, 1
	v_add3_u32 v2, v37, v2, s1
	v_bfe_u32 v15, v39, 16, 1
	v_lshrrev_b32_e32 v2, 16, v2
	v_add3_u32 v15, v39, v15, s1
	v_and_or_b32 v15, v15, s0, v2
	v_bfe_u32 v2, v41, 16, 1
	v_add3_u32 v2, v41, v2, s1
	v_bfe_u32 v16, v43, 16, 1
	v_lshrrev_b32_e32 v2, 16, v2
	v_add3_u32 v16, v43, v16, s1
	v_and_or_b32 v16, v16, s0, v2
	v_bfe_u32 v2, v45, 16, 1
	v_add3_u32 v2, v45, v2, s1
	v_bfe_u32 v17, v47, 16, 1
	v_lshrrev_b32_e32 v2, 16, v2
	v_add3_u32 v17, v47, v17, s1
	v_and_or_b32 v17, v17, s0, v2
	v_or_b32_e32 v2, s6, v22
	v_mul_hi_u32_u24_e32 v31, s8, v2
	v_mul_u32_u24_e32 v30, s8, v2
	ds_read2_b32 v[34:35], v21 offset0:16 offset1:24
	v_lshl_add_u64 v[30:31], v[30:31], 1, v[32:33]
	global_store_dwordx4 v[30:31], v[14:17], off
	ds_read2_b32 v[30:31], v21 offset0:49 offset1:57
	ds_read2_b32 v[36:37], v21 offset0:82 offset1:90
	ds_read2_b32 v[38:39], v21 offset0:115 offset1:123
	s_waitcnt lgkmcnt(3)
	v_bfe_u32 v2, v34, 16, 1
	v_add3_u32 v2, v34, v2, s1
	s_waitcnt lgkmcnt(2)
	v_bfe_u32 v14, v30, 16, 1
	ds_read2_b32 v[40:41], v21 offset0:148 offset1:156
	v_lshrrev_b32_e32 v2, 16, v2
	v_add3_u32 v14, v30, v14, s1
	ds_read2_b32 v[42:43], v21 offset0:181 offset1:189
	v_and_or_b32 v14, v14, s0, v2
	s_waitcnt lgkmcnt(3)
	v_bfe_u32 v2, v36, 16, 1
	v_add3_u32 v2, v36, v2, s1
	s_waitcnt lgkmcnt(2)
	v_bfe_u32 v15, v38, 16, 1
	ds_read2_b32 v[44:45], v21 offset0:214 offset1:222
	v_lshrrev_b32_e32 v2, 16, v2
	v_add3_u32 v15, v38, v15, s1
	ds_read2_b32 v[46:47], v21 offset0:247 offset1:255
	v_and_or_b32 v15, v15, s0, v2
	s_waitcnt lgkmcnt(3)
	v_bfe_u32 v2, v40, 16, 1
	v_add3_u32 v2, v40, v2, s1
	s_waitcnt lgkmcnt(2)
	v_bfe_u32 v16, v42, 16, 1
	v_lshrrev_b32_e32 v2, 16, v2
	v_add3_u32 v16, v42, v16, s1
	v_and_or_b32 v16, v16, s0, v2
	s_waitcnt lgkmcnt(1)
	v_bfe_u32 v2, v44, 16, 1
	v_add3_u32 v2, v44, v2, s1
	s_waitcnt lgkmcnt(0)
	v_bfe_u32 v17, v46, 16, 1
	v_lshrrev_b32_e32 v2, 16, v2
	v_add3_u32 v17, v46, v17, s1
	v_and_or_b32 v17, v17, s0, v2
	v_or_b32_e32 v2, s6, v23
	v_mul_hi_u32_u24_e32 v49, s8, v2
	v_mul_u32_u24_e32 v48, s8, v2
	v_lshl_add_u64 v[48:49], v[48:49], 1, v[32:33]
	v_bfe_u32 v2, v35, 16, 1
	global_store_dwordx4 v[48:49], v[14:17], off
	v_add3_u32 v2, v35, v2, s1
	v_lshrrev_b32_e32 v2, 16, v2
	v_bfe_u32 v14, v31, 16, 1
	v_add3_u32 v14, v31, v14, s1
	v_and_or_b32 v14, v14, s0, v2
	v_bfe_u32 v2, v37, 16, 1
	v_add3_u32 v2, v37, v2, s1
	v_bfe_u32 v15, v39, 16, 1
	v_lshrrev_b32_e32 v2, 16, v2
	v_add3_u32 v15, v39, v15, s1
	v_and_or_b32 v15, v15, s0, v2
	v_bfe_u32 v2, v41, 16, 1
	v_add3_u32 v2, v41, v2, s1
	v_bfe_u32 v16, v43, 16, 1
	v_lshrrev_b32_e32 v2, 16, v2
	v_add3_u32 v16, v43, v16, s1
	v_and_or_b32 v16, v16, s0, v2
	v_bfe_u32 v2, v45, 16, 1
	v_add3_u32 v2, v45, v2, s1
	v_bfe_u32 v17, v47, 16, 1
	v_lshrrev_b32_e32 v2, 16, v2
	v_add3_u32 v17, v47, v17, s1
	v_and_or_b32 v17, v17, s0, v2
	v_or_b32_e32 v2, s6, v24
	v_mul_hi_u32_u24_e32 v31, s8, v2
	v_mul_u32_u24_e32 v30, s8, v2
	v_lshl_add_u64 v[30:31], v[30:31], 1, v[32:33]
	global_store_dwordx4 v[30:31], v[14:17], off
	s_waitcnt lgkmcnt(0)
	s_mov_b32 s62, 0x18000
	s_mov_b32 s63, 0x1a000
	s_mov_b32 s77, 0xc000
	s_mov_b32 s76, 0xe000

.LBB0_87:
	v_or_b32_e32 v2, s6, v16
	s_or_b32 s7, s6, 2
	s_or_b32 s8, s6, 4
	v_lshlrev_b32_e32 v2, 10, v2
	v_or_b32_e32 v17, s7, v16
	s_or_b32 s9, s6, 6
	v_or_b32_e32 v29, s8, v16
	v_lshl_add_u64 v[30:31], v[2:3], 2, v[14:15]
	v_lshlrev_b32_e32 v2, 10, v17
	s_or_b32 s16, s6, 8
	v_or_b32_e32 v34, s9, v16
	v_lshl_add_u64 v[32:33], v[2:3], 2, v[14:15]
	v_lshlrev_b32_e32 v2, 10, v29
	s_or_b32 s17, s6, 10
	v_or_b32_e32 v35, s16, v16
	global_load_dword v17, v[30:31], off nt
	global_load_dword v29, v[32:33], off nt
	v_lshl_add_u64 v[30:31], v[2:3], 2, v[14:15]
	v_lshlrev_b32_e32 v2, 10, v34
	s_or_b32 s38, s6, 12
	v_or_b32_e32 v36, s17, v16
	v_lshl_add_u64 v[32:33], v[2:3], 2, v[14:15]
	v_lshlrev_b32_e32 v2, 10, v35
	s_or_b32 s39, s6, 14
	v_or_b32_e32 v37, s38, v16
	global_load_dword v34, v[30:31], off nt
	global_load_dword v35, v[32:33], off nt
	v_lshl_add_u64 v[30:31], v[2:3], 2, v[14:15]
	v_lshlrev_b32_e32 v2, 10, v36
	s_or_b32 s40, s6, 16
	v_or_b32_e32 v38, s39, v16
	v_lshl_add_u64 v[32:33], v[2:3], 2, v[14:15]
	v_lshlrev_b32_e32 v2, 10, v37
	s_or_b32 s41, s6, 18
	v_or_b32_e32 v39, s40, v16
	global_load_dword v36, v[30:31], off nt
	global_load_dword v37, v[32:33], off nt
	v_lshl_add_u64 v[30:31], v[2:3], 2, v[14:15]
	v_lshlrev_b32_e32 v2, 10, v38
	s_or_b32 s59, s6, 20
	v_or_b32_e32 v40, s41, v16
	v_lshl_add_u64 v[32:33], v[2:3], 2, v[14:15]
	v_lshlrev_b32_e32 v2, 10, v39
	s_or_b32 s62, s6, 22
	v_or_b32_e32 v41, s59, v16
	global_load_dword v38, v[30:31], off nt
	global_load_dword v39, v[32:33], off nt
	v_lshl_add_u64 v[30:31], v[2:3], 2, v[14:15]
	v_lshlrev_b32_e32 v2, 10, v40
	s_or_b32 s63, s6, 24
	v_or_b32_e32 v42, s62, v16
	v_lshl_add_u64 v[32:33], v[2:3], 2, v[14:15]
	v_lshlrev_b32_e32 v2, 10, v41
	s_or_b32 s68, s6, 26
	v_or_b32_e32 v43, s63, v16
	global_load_dword v40, v[30:31], off nt
	global_load_dword v41, v[32:33], off nt
	v_lshl_add_u64 v[30:31], v[2:3], 2, v[14:15]
	v_lshlrev_b32_e32 v2, 10, v42
	s_or_b32 s69, s6, 28
	v_or_b32_e32 v44, s68, v16
	v_lshl_add_u64 v[32:33], v[2:3], 2, v[14:15]
	v_lshlrev_b32_e32 v2, 10, v43
	s_or_b32 s74, s6, 30
	v_or_b32_e32 v45, s69, v16
	global_load_dword v42, v[30:31], off nt
	global_load_dword v43, v[32:33], off nt
	v_lshl_add_u64 v[30:31], v[2:3], 2, v[14:15]
	v_lshlrev_b32_e32 v2, 10, v44
	v_or_b32_e32 v46, s74, v16
	v_lshl_add_u64 v[32:33], v[2:3], 2, v[14:15]
	v_lshlrev_b32_e32 v2, 10, v45
	global_load_dword v44, v[30:31], off nt
	global_load_dword v45, v[32:33], off nt
	v_lshl_add_u64 v[30:31], v[2:3], 2, v[14:15]
	v_lshlrev_b32_e32 v2, 10, v46
	v_lshl_add_u64 v[32:33], v[2:3], 2, v[14:15]
	global_load_dword v2, v[30:31], off nt
	s_nop 0
	global_load_dword v30, v[32:33], off nt
	v_or_b32_e32 v31, s6, v18
	s_mov_b32 s6, 32
	s_and_b64 vcc, exec, s[36:37]
	s_mov_b64 s[36:37], 0
	v_mad_u32_u24 v31, v31, s66, v19
	v_or_b32_e32 v32, s7, v18
	v_or_b32_e32 v33, s8, v18
	v_or_b32_e32 v46, s9, v18
	v_or_b32_e32 v47, s16, v18
	v_or_b32_e32 v48, s17, v18
	v_or_b32_e32 v49, s38, v18
	v_or_b32_e32 v52, s39, v18
	v_or_b32_e32 v53, s40, v18
	v_or_b32_e32 v54, s41, v18
	v_or_b32_e32 v55, s59, v18
	v_or_b32_e32 v56, s62, v18
	v_or_b32_e32 v57, s63, v18
	v_or_b32_e32 v58, s68, v18
	v_or_b32_e32 v59, s69, v18
	v_or_b32_e32 v60, s74, v18
	v_mad_u32_u24 v32, v32, s66, v19
	v_mad_u32_u24 v33, v33, s66, v19
	v_mad_u32_u24 v46, v46, s66, v19
	v_mad_u32_u24 v47, v47, s66, v19
	v_mad_u32_u24 v48, v48, s66, v19
	v_mad_u32_u24 v49, v49, s66, v19
	v_mad_u32_u24 v52, v52, s66, v19
	v_mad_u32_u24 v53, v53, s66, v19
	v_mad_u32_u24 v54, v54, s66, v19
	v_mad_u32_u24 v55, v55, s66, v19
	v_mad_u32_u24 v56, v56, s66, v19
	v_mad_u32_u24 v57, v57, s66, v19
	v_mad_u32_u24 v58, v58, s66, v19
	v_mad_u32_u24 v59, v59, s66, v19
	v_mad_u32_u24 v60, v60, s66, v19
	s_waitcnt vmcnt(0)
	ds_write_b32 v31, v17
	s_waitcnt vmcnt(14)
	ds_write_b32 v32, v29
	s_waitcnt vmcnt(13)
	ds_write_b32 v33, v34
	s_waitcnt vmcnt(12)
	ds_write_b32 v46, v35
	s_waitcnt vmcnt(11)
	ds_write_b32 v47, v36
	s_waitcnt vmcnt(10)
	ds_write_b32 v48, v37
	s_waitcnt vmcnt(9)
	ds_write_b32 v49, v38
	s_waitcnt vmcnt(8)
	ds_write_b32 v52, v39
	s_waitcnt vmcnt(7)
	ds_write_b32 v53, v40
	s_waitcnt vmcnt(6)
	ds_write_b32 v54, v41
	s_waitcnt vmcnt(5)
	ds_write_b32 v55, v42
	s_waitcnt vmcnt(4)
	ds_write_b32 v56, v43
	s_waitcnt vmcnt(3)
	ds_write_b32 v57, v44
	s_waitcnt vmcnt(2)
	ds_write_b32 v58, v45
	s_waitcnt vmcnt(1)
	ds_write_b32 v59, v2
	s_waitcnt vmcnt(0)
	ds_write_b32 v60, v30
	s_cbranch_vccnz .LBB0_87
	s_waitcnt lgkmcnt(0)
	s_lshl_b64 s[6:7], s[56:57], 19
	ds_read2_b32 v[30:31], v21 offset1:8
	s_add_u32 s6, s19, s6
	ds_read2_b32 v[34:35], v21 offset0:33 offset1:41
	s_addc_u32 s7, s47, s7
	s_lshl_b32 s5, s5, 1
	s_add_u32 s6, s6, s5
	ds_read2_b32 v[36:37], v21 offset0:66 offset1:74
	s_addc_u32 s7, s7, 0
	v_lshlrev_b32_e32 v2, 1, v4
	ds_read2_b32 v[38:39], v21 offset0:99 offset1:107
	v_lshl_add_u64 v[32:33], s[6:7], 0, v[2:3]
	s_waitcnt lgkmcnt(3)
	v_bfe_u32 v2, v30, 16, 1
	v_add3_u32 v2, v30, v2, s1
	s_waitcnt lgkmcnt(2)
	v_bfe_u32 v14, v34, 16, 1
	ds_read2_b32 v[40:41], v21 offset0:132 offset1:140
	v_lshrrev_b32_e32 v2, 16, v2
	v_add3_u32 v14, v34, v14, s1
	ds_read2_b32 v[42:43], v21 offset0:165 offset1:173
	v_and_or_b32 v14, v14, s0, v2
	s_waitcnt lgkmcnt(3)
	v_bfe_u32 v2, v36, 16, 1
	v_add3_u32 v2, v36, v2, s1
	s_waitcnt lgkmcnt(2)
	v_bfe_u32 v15, v38, 16, 1
	ds_read2_b32 v[44:45], v21 offset0:198 offset1:206
	v_lshrrev_b32_e32 v2, 16, v2
	v_add3_u32 v15, v38, v15, s1
	ds_read2_b32 v[46:47], v21 offset0:231 offset1:239
	v_and_or_b32 v15, v15, s0, v2
	s_waitcnt lgkmcnt(3)
	v_bfe_u32 v2, v40, 16, 1
	v_add3_u32 v2, v40, v2, s1
	s_waitcnt lgkmcnt(2)
	v_bfe_u32 v16, v42, 16, 1
	v_lshrrev_b32_e32 v2, 16, v2
	v_add3_u32 v16, v42, v16, s1
	v_and_or_b32 v16, v16, s0, v2
	s_waitcnt lgkmcnt(1)
	v_bfe_u32 v2, v44, 16, 1
	v_add3_u32 v2, v44, v2, s1
	s_waitcnt lgkmcnt(0)
	v_bfe_u32 v17, v46, 16, 1
	v_lshrrev_b32_e32 v2, 16, v2
	v_add3_u32 v17, v46, v17, s1
	v_and_or_b32 v17, v17, s0, v2
	v_or_b32_e32 v2, s4, v20
	v_lshlrev_b32_e32 v2, 9, v2
	v_lshl_add_u64 v[48:49], v[32:33], 0, v[2:3]
	v_bfe_u32 v2, v31, 16, 1
	global_store_dwordx4 v[48:49], v[14:17], off
	v_add3_u32 v2, v31, v2, s1
	v_lshrrev_b32_e32 v2, 16, v2
	v_bfe_u32 v14, v35, 16, 1
	v_add3_u32 v14, v35, v14, s1
	v_and_or_b32 v14, v14, s0, v2
	v_bfe_u32 v2, v37, 16, 1
	v_add3_u32 v2, v37, v2, s1
	v_bfe_u32 v15, v39, 16, 1
	v_lshrrev_b32_e32 v2, 16, v2
	v_add3_u32 v15, v39, v15, s1
	v_and_or_b32 v15, v15, s0, v2
	v_bfe_u32 v2, v41, 16, 1
	v_add3_u32 v2, v41, v2, s1
	v_bfe_u32 v16, v43, 16, 1
	v_lshrrev_b32_e32 v2, 16, v2
	v_add3_u32 v16, v43, v16, s1
	v_and_or_b32 v16, v16, s0, v2
	v_bfe_u32 v2, v45, 16, 1
	v_add3_u32 v2, v45, v2, s1
	v_bfe_u32 v17, v47, 16, 1
	v_lshrrev_b32_e32 v2, 16, v2
	v_add3_u32 v17, v47, v17, s1
	v_and_or_b32 v17, v17, s0, v2
	v_or_b32_e32 v2, s4, v22
	v_lshlrev_b32_e32 v2, 9, v2
	ds_read2_b32 v[30:31], v21 offset0:16 offset1:24
	v_lshl_add_u64 v[34:35], v[32:33], 0, v[2:3]
	global_store_dwordx4 v[34:35], v[14:17], off
	ds_read2_b32 v[34:35], v21 offset0:49 offset1:57
	ds_read2_b32 v[36:37], v21 offset0:82 offset1:90
	ds_read2_b32 v[38:39], v21 offset0:115 offset1:123
	s_waitcnt lgkmcnt(3)
	v_bfe_u32 v2, v30, 16, 1
	v_add3_u32 v2, v30, v2, s1
	s_waitcnt lgkmcnt(2)
	v_bfe_u32 v14, v34, 16, 1
	ds_read2_b32 v[40:41], v21 offset0:148 offset1:156
	v_lshrrev_b32_e32 v2, 16, v2
	v_add3_u32 v14, v34, v14, s1
	ds_read2_b32 v[42:43], v21 offset0:181 offset1:189
	v_and_or_b32 v14, v14, s0, v2
	s_waitcnt lgkmcnt(3)
	v_bfe_u32 v2, v36, 16, 1
	v_add3_u32 v2, v36, v2, s1
	s_waitcnt lgkmcnt(2)
	v_bfe_u32 v15, v38, 16, 1
	ds_read2_b32 v[44:45], v21 offset0:214 offset1:222
	v_lshrrev_b32_e32 v2, 16, v2
	v_add3_u32 v15, v38, v15, s1
	ds_read2_b32 v[46:47], v21 offset0:247 offset1:255
	v_and_or_b32 v15, v15, s0, v2
	s_waitcnt lgkmcnt(3)
	v_bfe_u32 v2, v40, 16, 1
	v_add3_u32 v2, v40, v2, s1
	s_waitcnt lgkmcnt(2)
	v_bfe_u32 v16, v42, 16, 1
	v_lshrrev_b32_e32 v2, 16, v2
	v_add3_u32 v16, v42, v16, s1
	v_and_or_b32 v16, v16, s0, v2
	s_waitcnt lgkmcnt(1)
	v_bfe_u32 v2, v44, 16, 1
	v_add3_u32 v2, v44, v2, s1
	s_waitcnt lgkmcnt(0)
	v_bfe_u32 v17, v46, 16, 1
	v_lshrrev_b32_e32 v2, 16, v2
	v_add3_u32 v17, v46, v17, s1
	v_and_or_b32 v17, v17, s0, v2
	v_or_b32_e32 v2, s4, v23
	v_lshlrev_b32_e32 v2, 9, v2
	v_lshl_add_u64 v[48:49], v[32:33], 0, v[2:3]
	v_bfe_u32 v2, v31, 16, 1
	global_store_dwordx4 v[48:49], v[14:17], off
	v_add3_u32 v2, v31, v2, s1
	v_lshrrev_b32_e32 v2, 16, v2
	v_bfe_u32 v14, v35, 16, 1
	v_add3_u32 v14, v35, v14, s1
	v_and_or_b32 v14, v14, s0, v2
	v_bfe_u32 v2, v37, 16, 1
	v_add3_u32 v2, v37, v2, s1
	v_bfe_u32 v15, v39, 16, 1
	v_lshrrev_b32_e32 v2, 16, v2
	v_add3_u32 v15, v39, v15, s1
	v_and_or_b32 v15, v15, s0, v2
	v_bfe_u32 v2, v41, 16, 1
	v_add3_u32 v2, v41, v2, s1
	v_bfe_u32 v16, v43, 16, 1
	v_lshrrev_b32_e32 v2, 16, v2
	v_add3_u32 v16, v43, v16, s1
	v_and_or_b32 v16, v16, s0, v2
	v_bfe_u32 v2, v45, 16, 1
	v_add3_u32 v2, v45, v2, s1
	v_bfe_u32 v17, v47, 16, 1
	v_lshrrev_b32_e32 v2, 16, v2
	v_add3_u32 v17, v47, v17, s1
	v_and_or_b32 v17, v17, s0, v2
	v_or_b32_e32 v2, s4, v24
	v_lshlrev_b32_e32 v2, 9, v2
	v_lshl_add_u64 v[30:31], v[32:33], 0, v[2:3]
	global_store_dwordx4 v[30:31], v[14:17], off
	s_waitcnt lgkmcnt(0)
	s_mov_b32 s62, 0x18000
	s_mov_b32 s63, 0x1a000
	v_readlane_b32 s74, v255, 38

.LBB0_92:
	v_or_b32_e32 v2, s6, v29
	v_mov_b64_e32 v[30:31], s[22:23]
	v_mov_b32_e32 v15, v3
	s_or_b32 s7, s6, 2
	v_lshl_add_u64 v[32:33], v[2:3], 2, s[38:39]
	v_mad_u64_u32 v[34:35], s[76:77], v2, s26, v[30:31]
	v_mov_b32_e32 v17, v3
	v_or_b32_e32 v36, s7, v29
	global_load_dword v67, v[32:33], off nt
	v_lshl_add_u64 v[32:33], v[34:35], 0, v[14:15]
	s_or_b32 s8, s6, 4
	s_or_b32 s9, s6, 6
	s_or_b32 s16, s6, 8
	s_or_b32 s17, s6, 10
	s_or_b32 s36, s6, 12
	s_or_b32 s37, s6, 14
	s_or_b32 s56, s6, 16
	s_or_b32 s59, s6, 18
	s_or_b32 s62, s6, 20
	s_or_b32 s63, s6, 22
	s_or_b32 s68, s6, 24
	s_or_b32 s69, s6, 26
	s_or_b32 s74, s6, 28
	s_or_b32 s75, s6, 30
	v_add_u32_e32 v2, s6, v29
	v_mad_u64_u32 v[36:37], s[76:77], v36, s26, v[30:31]
	v_lshl_add_u64 v[32:33], v[32:33], 0, v[16:17]
	v_or_b32_e32 v38, s8, v29
	v_or_b32_e32 v40, s9, v29
	v_or_b32_e32 v42, s16, v29
	v_or_b32_e32 v44, s17, v29
	v_or_b32_e32 v46, s36, v29
	v_or_b32_e32 v48, s37, v29
	v_or_b32_e32 v52, s56, v29
	v_or_b32_e32 v54, s59, v29
	v_or_b32_e32 v56, s62, v29
	v_or_b32_e32 v58, s63, v29
	v_or_b32_e32 v60, s68, v29
	v_or_b32_e32 v62, s69, v29
	v_or_b32_e32 v64, s74, v29
	v_or_b32_e32 v66, s75, v29
	v_lshl_add_u64 v[34:35], v[2:3], 2, s[38:39]
	v_lshl_add_u64 v[36:37], v[36:37], 0, v[14:15]
	v_add_co_u32_e32 v32, vcc, 0x2000, v32
	v_mad_u64_u32 v[38:39], s[76:77], v38, s26, v[30:31]
	v_mad_u64_u32 v[40:41], s[76:77], v40, s26, v[30:31]
	v_mad_u64_u32 v[42:43], s[76:77], v42, s26, v[30:31]
	v_mad_u64_u32 v[44:45], s[76:77], v44, s26, v[30:31]
	v_mad_u64_u32 v[46:47], s[76:77], v46, s26, v[30:31]
	v_mad_u64_u32 v[48:49], s[76:77], v48, s26, v[30:31]
	v_mad_u64_u32 v[52:53], s[76:77], v52, s26, v[30:31]
	v_mad_u64_u32 v[54:55], s[76:77], v54, s26, v[30:31]
	v_mad_u64_u32 v[56:57], s[76:77], v56, s26, v[30:31]
	v_mad_u64_u32 v[58:59], s[76:77], v58, s26, v[30:31]
	v_mad_u64_u32 v[60:61], s[76:77], v60, s26, v[30:31]
	v_mad_u64_u32 v[62:63], s[76:77], v62, s26, v[30:31]
	v_mad_u64_u32 v[64:65], s[76:77], v64, s26, v[30:31]
	v_mad_u64_u32 v[30:31], s[76:77], v66, s26, v[30:31]
	global_load_dword v2, v[34:35], off offset:8 nt
	global_load_dword v66, v[34:35], off offset:16 nt
	global_load_dword v68, v[34:35], off offset:24 nt
	global_load_dword v69, v[34:35], off offset:32 nt
	global_load_dword v70, v[34:35], off offset:40 nt
	global_load_dword v71, v[34:35], off offset:48 nt
	global_load_dword v72, v[34:35], off offset:56 nt
	global_load_dword v73, v[34:35], off offset:64 nt
	global_load_dword v74, v[34:35], off offset:72 nt
	global_load_dword v75, v[34:35], off offset:80 nt
	global_load_dword v76, v[34:35], off offset:88 nt
	global_load_dword v77, v[34:35], off offset:96 nt
	global_load_dword v78, v[34:35], off offset:104 nt
	global_load_dword v79, v[34:35], off offset:112 nt
	global_load_dword v80, v[34:35], off offset:120 nt
	v_lshl_add_u64 v[34:35], v[36:37], 0, v[16:17]
	v_addc_co_u32_e32 v33, vcc, 0, v33, vcc
	v_lshl_add_u64 v[38:39], v[38:39], 0, v[14:15]
	v_add_co_u32_e32 v34, vcc, s27, v34
	v_lshl_add_u64 v[36:37], v[38:39], 0, v[16:17]
	s_nop 0
	v_addc_co_u32_e32 v35, vcc, 0, v35, vcc
	v_lshl_add_u64 v[40:41], v[40:41], 0, v[14:15]
	v_lshl_add_u64 v[42:43], v[42:43], 0, v[14:15]
	v_lshl_add_u64 v[44:45], v[44:45], 0, v[14:15]
	v_lshl_add_u64 v[46:47], v[46:47], 0, v[14:15]
	v_lshl_add_u64 v[48:49], v[48:49], 0, v[14:15]
	v_lshl_add_u64 v[52:53], v[52:53], 0, v[14:15]
	v_lshl_add_u64 v[54:55], v[54:55], 0, v[14:15]
	v_lshl_add_u64 v[56:57], v[56:57], 0, v[14:15]
	v_lshl_add_u64 v[58:59], v[58:59], 0, v[14:15]
	v_lshl_add_u64 v[60:61], v[60:61], 0, v[14:15]
	v_lshl_add_u64 v[62:63], v[62:63], 0, v[14:15]
	v_lshl_add_u64 v[64:65], v[64:65], 0, v[14:15]
	v_lshl_add_u64 v[30:31], v[30:31], 0, v[14:15]
	global_load_dword v15, v[32:33], off offset:2784 nt
	v_add_co_u32_e32 v32, vcc, s27, v36
	v_lshl_add_u64 v[38:39], v[40:41], 0, v[16:17]
	s_nop 0
	v_addc_co_u32_e32 v33, vcc, 0, v37, vcc
	v_add_co_u32_e32 v36, vcc, s27, v38
	v_lshl_add_u64 v[40:41], v[42:43], 0, v[16:17]
	s_nop 0
	v_addc_co_u32_e32 v37, vcc, 0, v39, vcc
	v_lshl_add_u64 v[42:43], v[44:45], 0, v[16:17]
	v_lshl_add_u64 v[44:45], v[46:47], 0, v[16:17]
	v_lshl_add_u64 v[46:47], v[48:49], 0, v[16:17]
	v_lshl_add_u64 v[48:49], v[52:53], 0, v[16:17]
	v_lshl_add_u64 v[52:53], v[54:55], 0, v[16:17]
	v_lshl_add_u64 v[54:55], v[56:57], 0, v[16:17]
	v_lshl_add_u64 v[56:57], v[58:59], 0, v[16:17]
	v_lshl_add_u64 v[58:59], v[60:61], 0, v[16:17]
	v_lshl_add_u64 v[60:61], v[62:63], 0, v[16:17]
	v_lshl_add_u64 v[62:63], v[64:65], 0, v[16:17]
	v_lshl_add_u64 v[30:31], v[30:31], 0, v[16:17]
	global_load_dword v17, v[34:35], off offset:2784 nt
	global_load_dword v38, v[32:33], off offset:2784 nt
	v_add_co_u32_e32 v32, vcc, s27, v40
	s_waitcnt vmcnt(0)
	v_mul_f32_e32 v15, v67, v15
	v_addc_co_u32_e32 v33, vcc, 0, v41, vcc
	v_add_co_u32_e32 v34, vcc, s27, v42
	global_load_dword v39, v[36:37], off offset:2784 nt
	global_load_dword v40, v[32:33], off offset:2784 nt
	v_addc_co_u32_e32 v35, vcc, 0, v43, vcc
	v_add_co_u32_e32 v32, vcc, s27, v44
	s_waitcnt vmcnt(3)
	v_mul_f32_e32 v2, v2, v17
	v_addc_co_u32_e32 v33, vcc, 0, v45, vcc
	v_add_co_u32_e32 v36, vcc, s27, v46
	global_load_dword v41, v[34:35], off offset:2784 nt
	global_load_dword v42, v[32:33], off offset:2784 nt
	v_addc_co_u32_e32 v37, vcc, 0, v47, vcc
	v_add_co_u32_e32 v32, vcc, s27, v48
	v_or_b32_e32 v47, s9, v18
	s_nop 0
	v_addc_co_u32_e32 v33, vcc, 0, v49, vcc
	v_add_co_u32_e32 v34, vcc, s27, v52
	global_load_dword v43, v[36:37], off offset:2784 nt
	global_load_dword v44, v[32:33], off offset:2784 nt
	v_addc_co_u32_e32 v35, vcc, 0, v53, vcc
	v_add_co_u32_e32 v32, vcc, s27, v54
	v_or_b32_e32 v48, s16, v18
	s_nop 0
	v_addc_co_u32_e32 v33, vcc, 0, v55, vcc
	v_add_co_u32_e32 v36, vcc, s27, v56
	global_load_dword v45, v[34:35], off offset:2784 nt
	global_load_dword v46, v[32:33], off offset:2784 nt
	v_addc_co_u32_e32 v37, vcc, 0, v57, vcc
	v_add_co_u32_e32 v32, vcc, s27, v58
	v_or_b32_e32 v49, s17, v18
	s_nop 0
	v_addc_co_u32_e32 v33, vcc, 0, v59, vcc
	v_add_co_u32_e32 v34, vcc, s27, v60
	global_load_dword v36, v[36:37], off offset:2784 nt
	s_nop 0
	global_load_dword v37, v[32:33], off offset:2784 nt
	v_addc_co_u32_e32 v35, vcc, 0, v61, vcc
	v_add_co_u32_e32 v32, vcc, s27, v62
	v_or_b32_e32 v52, s36, v18
	s_nop 0
	v_addc_co_u32_e32 v33, vcc, 0, v63, vcc
	v_add_co_u32_e32 v30, vcc, s27, v30
	global_load_dword v34, v[34:35], off offset:2784 nt
	s_nop 0
	global_load_dword v32, v[32:33], off offset:2784 nt
	v_addc_co_u32_e32 v31, vcc, 0, v31, vcc
	global_load_dword v30, v[30:31], off offset:2784 nt
	v_or_b32_e32 v31, s6, v18
	v_mad_u32_u24 v31, v31, s66, v19
	v_or_b32_e32 v33, s7, v18
	v_or_b32_e32 v35, s8, v18
	v_mad_u32_u24 v33, v33, s66, v19
	v_mad_u32_u24 v35, v35, s66, v19
	ds_write_b32 v31, v15
	s_waitcnt vmcnt(13)
	v_mul_f32_e32 v15, v66, v38
	v_mad_u32_u24 v47, v47, s66, v19
	v_mad_u32_u24 v48, v48, s66, v19
	ds_write_b32 v33, v2
	ds_write_b32 v35, v15
	v_or_b32_e32 v53, s37, v18
	v_or_b32_e32 v54, s56, v18
	s_waitcnt vmcnt(12)
	v_mul_f32_e32 v2, v68, v39
	s_waitcnt vmcnt(11)
	v_mul_f32_e32 v15, v69, v40
	v_mad_u32_u24 v49, v49, s66, v19
	v_mad_u32_u24 v52, v52, s66, v19
	ds_write_b32 v47, v2
	ds_write_b32 v48, v15
	v_or_b32_e32 v55, s59, v18
	v_or_b32_e32 v56, s62, v18
	v_mad_u32_u24 v53, v53, s66, v19
	v_mad_u32_u24 v54, v54, s66, v19
	v_or_b32_e32 v57, s63, v18
	v_or_b32_e32 v58, s68, v18
	v_mad_u32_u24 v55, v55, s66, v19
	v_mad_u32_u24 v56, v56, s66, v19
	v_or_b32_e32 v59, s69, v18
	v_or_b32_e32 v60, s74, v18
	v_mad_u32_u24 v57, v57, s66, v19
	v_mad_u32_u24 v58, v58, s66, v19
	s_and_b64 vcc, exec, s[40:41]
	s_mov_b64 s[40:41], 0
	v_or_b32_e32 v61, s75, v18
	s_waitcnt vmcnt(10)
	v_mul_f32_e32 v2, v70, v41
	s_waitcnt vmcnt(9)
	v_mul_f32_e32 v15, v71, v42
	ds_write_b32 v49, v2
	ds_write_b32 v52, v15
	s_mov_b32 s6, 32
	v_mad_u32_u24 v59, v59, s66, v19
	v_mad_u32_u24 v60, v60, s66, v19
	v_mad_u32_u24 v61, v61, s66, v19
	s_waitcnt vmcnt(8)
	v_mul_f32_e32 v2, v72, v43
	s_waitcnt vmcnt(7)
	v_mul_f32_e32 v15, v73, v44
	ds_write_b32 v53, v2
	ds_write_b32 v54, v15
	s_waitcnt vmcnt(6)
	v_mul_f32_e32 v2, v74, v45
	s_waitcnt vmcnt(5)
	v_mul_f32_e32 v15, v75, v46
	ds_write_b32 v55, v2
	ds_write_b32 v56, v15
	s_waitcnt vmcnt(4)
	v_mul_f32_e32 v2, v76, v36
	s_waitcnt vmcnt(3)
	v_mul_f32_e32 v15, v77, v37
	ds_write_b32 v57, v2
	ds_write_b32 v58, v15
	s_waitcnt vmcnt(2)
	v_mul_f32_e32 v2, v78, v34
	s_waitcnt vmcnt(1)
	v_mul_f32_e32 v15, v79, v32
	ds_write_b32 v59, v2
	s_waitcnt vmcnt(0)
	v_mul_f32_e32 v2, v80, v30
	ds_write_b32 v60, v15
	ds_write_b32 v61, v2
	s_cbranch_vccnz .LBB0_92
	s_waitcnt lgkmcnt(0)
	ds_read2_b32 v[30:31], v21 offset1:8
	ds_read2_b32 v[34:35], v21 offset0:33 offset1:41
	ds_read2_b32 v[36:37], v21 offset0:66 offset1:74
	ds_read2_b32 v[38:39], v21 offset0:99 offset1:107
	ds_read2_b32 v[40:41], v21 offset0:132 offset1:140
	s_waitcnt lgkmcnt(4)
	v_bfe_u32 v2, v30, 16, 1
	v_add3_u32 v2, v30, v2, s1
	s_waitcnt lgkmcnt(3)
	v_bfe_u32 v14, v34, 16, 1
	v_lshrrev_b32_e32 v2, 16, v2
	v_add3_u32 v14, v34, v14, s1
	ds_read2_b32 v[42:43], v21 offset0:165 offset1:173
	v_and_or_b32 v14, v14, s0, v2
	s_waitcnt lgkmcnt(3)
	v_bfe_u32 v2, v36, 16, 1
	v_add3_u32 v2, v36, v2, s1
	s_waitcnt lgkmcnt(2)
	v_bfe_u32 v15, v38, 16, 1
	ds_read2_b32 v[44:45], v21 offset0:198 offset1:206
	v_lshrrev_b32_e32 v2, 16, v2
	v_add3_u32 v15, v38, v15, s1
	ds_read2_b32 v[46:47], v21 offset0:231 offset1:239
	v_and_or_b32 v15, v15, s0, v2
	s_waitcnt lgkmcnt(3)
	v_bfe_u32 v2, v40, 16, 1
	v_add3_u32 v2, v40, v2, s1
	s_waitcnt lgkmcnt(2)
	v_bfe_u32 v16, v42, 16, 1
	v_lshrrev_b32_e32 v2, 16, v2
	v_add3_u32 v16, v42, v16, s1
	v_and_or_b32 v16, v16, s0, v2
	s_waitcnt lgkmcnt(1)
	v_bfe_u32 v2, v44, 16, 1
	v_add3_u32 v2, v44, v2, s1
	s_waitcnt lgkmcnt(0)
	v_bfe_u32 v17, v46, 16, 1
	s_and_b32 s4, s4, 0x7fffffe0
	v_lshrrev_b32_e32 v2, 16, v2
	v_add3_u32 v17, v46, v17, s1
	s_lshl_b32 s56, s5, 1
	v_and_or_b32 v17, v17, s0, v2
	v_or_b32_e32 v2, s4, v20
	v_lshl_add_u64 v[32:33], v[6:7], 0, s[56:57]
	v_lshlrev_b32_e32 v2, 11, v2
	v_lshl_add_u64 v[48:49], v[32:33], 0, v[2:3]
	v_bfe_u32 v2, v31, 16, 1
	global_store_dwordx4 v[48:49], v[14:17], off
	v_add3_u32 v2, v31, v2, s1
	v_lshrrev_b32_e32 v2, 16, v2
	v_bfe_u32 v14, v35, 16, 1
	v_add3_u32 v14, v35, v14, s1
	v_and_or_b32 v14, v14, s0, v2
	v_bfe_u32 v2, v37, 16, 1
	v_add3_u32 v2, v37, v2, s1
	v_bfe_u32 v15, v39, 16, 1
	v_lshrrev_b32_e32 v2, 16, v2
	v_add3_u32 v15, v39, v15, s1
	v_and_or_b32 v15, v15, s0, v2
	v_bfe_u32 v2, v41, 16, 1
	v_add3_u32 v2, v41, v2, s1
	v_bfe_u32 v16, v43, 16, 1
	v_lshrrev_b32_e32 v2, 16, v2
	v_add3_u32 v16, v43, v16, s1
	v_and_or_b32 v16, v16, s0, v2
	v_bfe_u32 v2, v45, 16, 1
	v_add3_u32 v2, v45, v2, s1
	v_bfe_u32 v17, v47, 16, 1
	v_lshrrev_b32_e32 v2, 16, v2
	v_add3_u32 v17, v47, v17, s1
	v_and_or_b32 v17, v17, s0, v2
	v_or_b32_e32 v2, s4, v22
	v_lshlrev_b32_e32 v2, 11, v2
	ds_read2_b32 v[30:31], v21 offset0:16 offset1:24
	v_lshl_add_u64 v[34:35], v[32:33], 0, v[2:3]
	global_store_dwordx4 v[34:35], v[14:17], off
	ds_read2_b32 v[34:35], v21 offset0:49 offset1:57
	ds_read2_b32 v[36:37], v21 offset0:82 offset1:90
	ds_read2_b32 v[38:39], v21 offset0:115 offset1:123
	s_waitcnt lgkmcnt(3)
	v_bfe_u32 v2, v30, 16, 1
	v_add3_u32 v2, v30, v2, s1
	s_waitcnt lgkmcnt(2)
	v_bfe_u32 v14, v34, 16, 1
	ds_read2_b32 v[40:41], v21 offset0:148 offset1:156
	v_lshrrev_b32_e32 v2, 16, v2
	v_add3_u32 v14, v34, v14, s1
	ds_read2_b32 v[42:43], v21 offset0:181 offset1:189
	v_and_or_b32 v14, v14, s0, v2
	s_waitcnt lgkmcnt(3)
	v_bfe_u32 v2, v36, 16, 1
	v_add3_u32 v2, v36, v2, s1
	s_waitcnt lgkmcnt(2)
	v_bfe_u32 v15, v38, 16, 1
	ds_read2_b32 v[44:45], v21 offset0:214 offset1:222
	v_lshrrev_b32_e32 v2, 16, v2
	v_add3_u32 v15, v38, v15, s1
	ds_read2_b32 v[46:47], v21 offset0:247 offset1:255
	v_and_or_b32 v15, v15, s0, v2
	s_waitcnt lgkmcnt(3)
	v_bfe_u32 v2, v40, 16, 1
	v_add3_u32 v2, v40, v2, s1
	s_waitcnt lgkmcnt(2)
	v_bfe_u32 v16, v42, 16, 1
	v_lshrrev_b32_e32 v2, 16, v2
	v_add3_u32 v16, v42, v16, s1
	v_and_or_b32 v16, v16, s0, v2
	s_waitcnt lgkmcnt(1)
	v_bfe_u32 v2, v44, 16, 1
	v_add3_u32 v2, v44, v2, s1
	s_waitcnt lgkmcnt(0)
	v_bfe_u32 v17, v46, 16, 1
	v_lshrrev_b32_e32 v2, 16, v2
	v_add3_u32 v17, v46, v17, s1
	v_and_or_b32 v17, v17, s0, v2
	v_or_b32_e32 v2, s4, v23
	v_lshlrev_b32_e32 v2, 11, v2
	v_lshl_add_u64 v[48:49], v[32:33], 0, v[2:3]
	v_bfe_u32 v2, v31, 16, 1
	global_store_dwordx4 v[48:49], v[14:17], off
	v_add3_u32 v2, v31, v2, s1
	v_lshrrev_b32_e32 v2, 16, v2
	v_bfe_u32 v14, v35, 16, 1
	v_add3_u32 v14, v35, v14, s1
	v_and_or_b32 v14, v14, s0, v2
	v_bfe_u32 v2, v37, 16, 1
	v_add3_u32 v2, v37, v2, s1
	v_bfe_u32 v15, v39, 16, 1
	v_lshrrev_b32_e32 v2, 16, v2
	v_add3_u32 v15, v39, v15, s1
	v_and_or_b32 v15, v15, s0, v2
	v_bfe_u32 v2, v41, 16, 1
	v_add3_u32 v2, v41, v2, s1
	v_bfe_u32 v16, v43, 16, 1
	v_lshrrev_b32_e32 v2, 16, v2
	v_add3_u32 v16, v43, v16, s1
	v_and_or_b32 v16, v16, s0, v2
	v_bfe_u32 v2, v45, 16, 1
	v_add3_u32 v2, v45, v2, s1
	v_bfe_u32 v17, v47, 16, 1
	v_lshrrev_b32_e32 v2, 16, v2
	v_add3_u32 v17, v47, v17, s1
	v_and_or_b32 v17, v17, s0, v2
	v_or_b32_e32 v2, s4, v24
	v_lshlrev_b32_e32 v2, 11, v2
	v_lshl_add_u64 v[30:31], v[32:33], 0, v[2:3]
	global_store_dwordx4 v[30:31], v[14:17], off
	s_waitcnt lgkmcnt(0)
	s_mov_b32 s62, 0x18000
	s_mov_b32 s63, 0x1a000
	s_mov_b32 s77, 0xc000
	s_mov_b32 s76, 0xe000
	s_movk_i32 s75, 0x3400
	v_readlane_b32 s74, v255, 38

.LBB0_109:
	v_or_b32_e32 v2, s4, v14
	s_or_b32 s5, s4, 2
	v_lshl_add_u64 v[16:17], v[2:3], 2, s[38:39]
	v_lshl_or_b32 v2, v2, 9, v15
	s_or_b32 s8, s4, 4
	v_or_b32_e32 v29, s5, v14
	global_load_dword v46, v[16:17], off nt
	v_lshl_add_u64 v[16:17], v[2:3], 2, s[36:37]
	v_add_u32_e32 v2, s4, v14
	s_or_b32 s9, s4, 6
	v_or_b32_e32 v32, s8, v14
	global_load_dword v47, v[16:17], off nt
	v_lshl_add_u64 v[16:17], v[2:3], 2, s[38:39]
	v_lshl_or_b32 v2, v29, 9, v15
	s_or_b32 s16, s4, 8
	v_or_b32_e32 v33, s9, v14
	v_lshl_add_u64 v[30:31], v[2:3], 2, s[36:37]
	v_lshl_or_b32 v2, v32, 9, v15
	s_or_b32 s17, s4, 10
	v_or_b32_e32 v34, s16, v14
	global_load_dword v29, v[16:17], off offset:8 nt
	global_load_dword v32, v[16:17], off offset:16 nt
	global_load_dword v48, v[16:17], off offset:24 nt
	global_load_dword v49, v[16:17], off offset:32 nt
	global_load_dword v52, v[16:17], off offset:40 nt
	global_load_dword v53, v[16:17], off offset:48 nt
	global_load_dword v54, v[16:17], off offset:56 nt
	global_load_dword v55, v[16:17], off offset:64 nt
	global_load_dword v56, v[16:17], off offset:72 nt
	global_load_dword v57, v[16:17], off offset:80 nt
	global_load_dword v58, v[16:17], off offset:88 nt
	global_load_dword v59, v[16:17], off offset:96 nt
	global_load_dword v60, v[16:17], off offset:104 nt
	global_load_dword v61, v[16:17], off offset:112 nt
	global_load_dword v62, v[16:17], off offset:120 nt
	v_lshl_add_u64 v[16:17], v[2:3], 2, s[36:37]
	v_lshl_or_b32 v2, v33, 9, v15
	s_or_b32 s56, s4, 12
	v_or_b32_e32 v35, s17, v14
	global_load_dword v33, v[30:31], off nt
	global_load_dword v63, v[16:17], off nt
	v_lshl_add_u64 v[16:17], v[2:3], 2, s[36:37]
	v_lshl_or_b32 v2, v34, 9, v15
	s_or_b32 s59, s4, 14
	v_or_b32_e32 v36, s56, v14
	v_lshl_add_u64 v[30:31], v[2:3], 2, s[36:37]
	v_lshl_or_b32 v2, v35, 9, v15
	s_or_b32 s62, s4, 16
	v_or_b32_e32 v37, s59, v14
	global_load_dword v34, v[16:17], off nt
	global_load_dword v35, v[30:31], off nt
	v_lshl_add_u64 v[16:17], v[2:3], 2, s[36:37]
	v_lshl_or_b32 v2, v36, 9, v15
	s_or_b32 s63, s4, 18
	v_or_b32_e32 v38, s62, v14
	v_lshl_add_u64 v[30:31], v[2:3], 2, s[36:37]
	v_lshl_or_b32 v2, v37, 9, v15
	s_or_b32 s68, s4, 20
	v_or_b32_e32 v39, s63, v14
	global_load_dword v36, v[16:17], off nt
	global_load_dword v37, v[30:31], off nt
	v_lshl_add_u64 v[16:17], v[2:3], 2, s[36:37]
	v_lshl_or_b32 v2, v38, 9, v15
	s_or_b32 s69, s4, 22
	v_or_b32_e32 v40, s68, v14
	v_lshl_add_u64 v[30:31], v[2:3], 2, s[36:37]
	v_lshl_or_b32 v2, v39, 9, v15
	s_or_b32 s74, s4, 24
	v_or_b32_e32 v41, s69, v14
	global_load_dword v38, v[16:17], off nt
	global_load_dword v39, v[30:31], off nt
	v_lshl_add_u64 v[16:17], v[2:3], 2, s[36:37]
	v_lshl_or_b32 v2, v40, 9, v15
	s_or_b32 s75, s4, 26
	v_or_b32_e32 v42, s74, v14
	global_load_dword v40, v[16:17], off nt
	v_lshl_add_u64 v[16:17], v[2:3], 2, s[36:37]
	v_lshl_or_b32 v2, v41, 9, v15
	s_or_b32 s76, s4, 28
	v_or_b32_e32 v43, s75, v14
	v_lshl_add_u64 v[30:31], v[2:3], 2, s[36:37]
	v_lshl_or_b32 v2, v42, 9, v15
	s_or_b32 s77, s4, 30
	v_or_b32_e32 v44, s76, v14
	global_load_dword v41, v[16:17], off nt
	global_load_dword v42, v[30:31], off nt
	v_lshl_add_u64 v[16:17], v[2:3], 2, s[36:37]
	v_lshl_or_b32 v2, v43, 9, v15
	v_or_b32_e32 v45, s77, v14
	v_lshl_add_u64 v[30:31], v[2:3], 2, s[36:37]
	v_lshl_or_b32 v2, v44, 9, v15
	global_load_dword v43, v[16:17], off nt
	s_nop 0
	global_load_dword v30, v[30:31], off nt
	v_lshl_add_u64 v[16:17], v[2:3], 2, s[36:37]
	v_lshl_or_b32 v2, v45, 9, v15
	global_load_dword v31, v[16:17], off nt
	v_lshl_add_u64 v[16:17], v[2:3], 2, s[36:37]
	global_load_dword v2, v[16:17], off nt
	v_or_b32_e32 v16, s4, v18
	v_mad_u32_u24 v16, v16, s66, v19
	v_or_b32_e32 v17, s5, v18
	v_or_b32_e32 v44, s8, v18
	v_or_b32_e32 v45, s9, v18
	v_or_b32_e32 v64, s16, v18
	v_mad_u32_u24 v17, v17, s66, v19
	v_or_b32_e32 v65, s17, v18
	v_or_b32_e32 v66, s56, v18
	v_mad_u32_u24 v44, v44, s66, v19
	v_mad_u32_u24 v45, v45, s66, v19
	v_mad_u32_u24 v64, v64, s66, v19
	v_or_b32_e32 v67, s59, v18
	s_waitcnt vmcnt(0)
	v_mul_f32_e32 v46, v46, v47
	ds_write_b32 v16, v46
	v_or_b32_e32 v68, s62, v18
	v_mad_u32_u24 v65, v65, s66, v19
	v_mad_u32_u24 v66, v66, s66, v19
	v_or_b32_e32 v69, s63, v18
	v_or_b32_e32 v70, s68, v18
	v_mad_u32_u24 v67, v67, s66, v19
	v_mad_u32_u24 v68, v68, s66, v19
	v_or_b32_e32 v71, s69, v18
	v_or_b32_e32 v72, s74, v18
	v_mad_u32_u24 v69, v69, s66, v19
	v_mad_u32_u24 v70, v70, s66, v19
	s_waitcnt vmcnt(14)
	v_mul_f32_e32 v16, v29, v33
	s_waitcnt vmcnt(13)
	v_mul_f32_e32 v29, v32, v63
	ds_write_b32 v17, v16
	ds_write_b32 v44, v29
	v_or_b32_e32 v73, s75, v18
	v_or_b32_e32 v74, s76, v18
	v_mad_u32_u24 v71, v71, s66, v19
	v_mad_u32_u24 v72, v72, s66, v19
	s_and_b64 vcc, exec, s[40:41]
	s_waitcnt vmcnt(12)
	v_mul_f32_e32 v16, v48, v34
	s_waitcnt vmcnt(11)
	v_mul_f32_e32 v17, v49, v35
	ds_write_b32 v45, v16
	ds_write_b32 v64, v17
	s_mov_b64 s[40:41], 0
	v_or_b32_e32 v75, s77, v18
	v_mad_u32_u24 v73, v73, s66, v19
	v_mad_u32_u24 v74, v74, s66, v19
	s_mov_b32 s4, 32
	s_waitcnt vmcnt(10)
	v_mul_f32_e32 v16, v52, v36
	s_waitcnt vmcnt(9)
	v_mul_f32_e32 v17, v53, v37
	ds_write_b32 v65, v16
	ds_write_b32 v66, v17
	v_mad_u32_u24 v75, v75, s66, v19
	s_waitcnt vmcnt(8)
	v_mul_f32_e32 v16, v54, v38
	s_waitcnt vmcnt(7)
	v_mul_f32_e32 v17, v55, v39
	ds_write_b32 v67, v16
	ds_write_b32 v68, v17
	s_waitcnt vmcnt(6)
	v_mul_f32_e32 v16, v56, v40
	ds_write_b32 v69, v16
	s_waitcnt vmcnt(5)
	v_mul_f32_e32 v17, v57, v41
	s_waitcnt vmcnt(4)
	v_mul_f32_e32 v16, v58, v42
	ds_write_b32 v70, v17
	ds_write_b32 v71, v16
	s_waitcnt vmcnt(3)
	v_mul_f32_e32 v17, v59, v43
	s_waitcnt vmcnt(2)
	v_mul_f32_e32 v16, v60, v30
	ds_write_b32 v72, v17
	ds_write_b32 v73, v16
	s_waitcnt vmcnt(1)
	v_mul_f32_e32 v17, v61, v31
	s_waitcnt vmcnt(0)
	v_mul_f32_e32 v2, v62, v2
	ds_write_b32 v74, v17
	ds_write_b32 v75, v2
	s_cbranch_vccnz .LBB0_109
	s_waitcnt lgkmcnt(0)
	ds_read2_b32 v[30:31], v21 offset1:8
	ds_read2_b32 v[34:35], v21 offset0:33 offset1:41
	ds_read2_b32 v[36:37], v21 offset0:66 offset1:74
	ds_read2_b32 v[38:39], v21 offset0:99 offset1:107
	ds_read2_b32 v[40:41], v21 offset0:132 offset1:140
	ds_read2_b32 v[42:43], v21 offset0:165 offset1:173
	s_waitcnt lgkmcnt(5)
	v_bfe_u32 v2, v30, 16, 1
	v_add3_u32 v2, v30, v2, s1
	s_waitcnt lgkmcnt(4)
	v_bfe_u32 v14, v34, 16, 1
	v_lshrrev_b32_e32 v2, 16, v2
	v_add3_u32 v14, v34, v14, s1
	v_and_or_b32 v14, v14, s0, v2
	s_waitcnt lgkmcnt(3)
	v_bfe_u32 v2, v36, 16, 1
	v_add3_u32 v2, v36, v2, s1
	s_waitcnt lgkmcnt(2)
	v_bfe_u32 v15, v38, 16, 1
	ds_read2_b32 v[44:45], v21 offset0:198 offset1:206
	v_lshrrev_b32_e32 v2, 16, v2
	v_add3_u32 v15, v38, v15, s1
	ds_read2_b32 v[46:47], v21 offset0:231 offset1:239
	v_and_or_b32 v15, v15, s0, v2
	s_waitcnt lgkmcnt(3)
	v_bfe_u32 v2, v40, 16, 1
	v_add3_u32 v2, v40, v2, s1
	s_waitcnt lgkmcnt(2)
	v_bfe_u32 v16, v42, 16, 1
	v_lshrrev_b32_e32 v2, 16, v2
	v_add3_u32 v16, v42, v16, s1
	v_and_or_b32 v16, v16, s0, v2
	s_waitcnt lgkmcnt(1)
	v_bfe_u32 v2, v44, 16, 1
	v_add3_u32 v2, v44, v2, s1
	s_waitcnt lgkmcnt(0)
	v_bfe_u32 v17, v46, 16, 1
	v_lshrrev_b32_e32 v2, 16, v2
	v_add3_u32 v17, v46, v17, s1
	s_lshl_b32 s56, s7, 1
	v_and_or_b32 v17, v17, s0, v2
	v_or_b32_e32 v2, s6, v20
	v_lshl_add_u64 v[32:33], v[8:9], 0, s[56:57]
	v_lshlrev_b32_e32 v2, 10, v2
	v_lshl_add_u64 v[48:49], v[32:33], 0, v[2:3]
	v_bfe_u32 v2, v31, 16, 1
	global_store_dwordx4 v[48:49], v[14:17], off
	v_add3_u32 v2, v31, v2, s1
	v_lshrrev_b32_e32 v2, 16, v2
	v_bfe_u32 v14, v35, 16, 1
	v_add3_u32 v14, v35, v14, s1
	v_and_or_b32 v14, v14, s0, v2
	v_bfe_u32 v2, v37, 16, 1
	v_add3_u32 v2, v37, v2, s1
	v_bfe_u32 v15, v39, 16, 1
	v_lshrrev_b32_e32 v2, 16, v2
	v_add3_u32 v15, v39, v15, s1
	v_and_or_b32 v15, v15, s0, v2
	v_bfe_u32 v2, v41, 16, 1
	v_add3_u32 v2, v41, v2, s1
	v_bfe_u32 v16, v43, 16, 1
	v_lshrrev_b32_e32 v2, 16, v2
	v_add3_u32 v16, v43, v16, s1
	v_and_or_b32 v16, v16, s0, v2
	v_bfe_u32 v2, v45, 16, 1
	v_add3_u32 v2, v45, v2, s1
	v_bfe_u32 v17, v47, 16, 1
	v_lshrrev_b32_e32 v2, 16, v2
	v_add3_u32 v17, v47, v17, s1
	v_and_or_b32 v17, v17, s0, v2
	v_or_b32_e32 v2, s6, v22
	v_lshlrev_b32_e32 v2, 10, v2
	ds_read2_b32 v[30:31], v21 offset0:16 offset1:24
	v_lshl_add_u64 v[34:35], v[32:33], 0, v[2:3]
	global_store_dwordx4 v[34:35], v[14:17], off
	ds_read2_b32 v[34:35], v21 offset0:49 offset1:57
	ds_read2_b32 v[36:37], v21 offset0:82 offset1:90
	ds_read2_b32 v[38:39], v21 offset0:115 offset1:123
	s_waitcnt lgkmcnt(3)
	v_bfe_u32 v2, v30, 16, 1
	v_add3_u32 v2, v30, v2, s1
	s_waitcnt lgkmcnt(2)
	v_bfe_u32 v14, v34, 16, 1
	ds_read2_b32 v[40:41], v21 offset0:148 offset1:156
	v_lshrrev_b32_e32 v2, 16, v2
	v_add3_u32 v14, v34, v14, s1
	ds_read2_b32 v[42:43], v21 offset0:181 offset1:189
	v_and_or_b32 v14, v14, s0, v2
	s_waitcnt lgkmcnt(3)
	v_bfe_u32 v2, v36, 16, 1
	v_add3_u32 v2, v36, v2, s1
	s_waitcnt lgkmcnt(2)
	v_bfe_u32 v15, v38, 16, 1
	ds_read2_b32 v[44:45], v21 offset0:214 offset1:222
	v_lshrrev_b32_e32 v2, 16, v2
	v_add3_u32 v15, v38, v15, s1
	ds_read2_b32 v[46:47], v21 offset0:247 offset1:255
	v_and_or_b32 v15, v15, s0, v2
	s_waitcnt lgkmcnt(3)
	v_bfe_u32 v2, v40, 16, 1
	v_add3_u32 v2, v40, v2, s1
	s_waitcnt lgkmcnt(2)
	v_bfe_u32 v16, v42, 16, 1
	v_lshrrev_b32_e32 v2, 16, v2
	v_add3_u32 v16, v42, v16, s1
	v_and_or_b32 v16, v16, s0, v2
	s_waitcnt lgkmcnt(1)
	v_bfe_u32 v2, v44, 16, 1
	v_add3_u32 v2, v44, v2, s1
	s_waitcnt lgkmcnt(0)
	v_bfe_u32 v17, v46, 16, 1
	v_lshrrev_b32_e32 v2, 16, v2
	v_add3_u32 v17, v46, v17, s1
	v_and_or_b32 v17, v17, s0, v2
	v_or_b32_e32 v2, s6, v23
	v_lshlrev_b32_e32 v2, 10, v2
	v_lshl_add_u64 v[48:49], v[32:33], 0, v[2:3]
	v_bfe_u32 v2, v31, 16, 1
	global_store_dwordx4 v[48:49], v[14:17], off
	v_add3_u32 v2, v31, v2, s1
	v_lshrrev_b32_e32 v2, 16, v2
	v_bfe_u32 v14, v35, 16, 1
	v_add3_u32 v14, v35, v14, s1
	v_and_or_b32 v14, v14, s0, v2
	v_bfe_u32 v2, v37, 16, 1
	v_add3_u32 v2, v37, v2, s1
	v_bfe_u32 v15, v39, 16, 1
	v_lshrrev_b32_e32 v2, 16, v2
	v_add3_u32 v15, v39, v15, s1
	v_and_or_b32 v15, v15, s0, v2
	v_bfe_u32 v2, v41, 16, 1
	v_add3_u32 v2, v41, v2, s1
	v_bfe_u32 v16, v43, 16, 1
	v_lshrrev_b32_e32 v2, 16, v2
	v_add3_u32 v16, v43, v16, s1
	v_and_or_b32 v16, v16, s0, v2
	v_bfe_u32 v2, v45, 16, 1
	v_add3_u32 v2, v45, v2, s1
	v_bfe_u32 v17, v47, 16, 1
	v_lshrrev_b32_e32 v2, 16, v2
	v_add3_u32 v17, v47, v17, s1
	v_and_or_b32 v17, v17, s0, v2
	v_or_b32_e32 v2, s6, v24
	v_lshlrev_b32_e32 v2, 10, v2
	v_lshl_add_u64 v[30:31], v[32:33], 0, v[2:3]
	global_store_dwordx4 v[30:31], v[14:17], off
	s_waitcnt lgkmcnt(0)
	s_mov_b32 s62, 0x18000
	s_mov_b32 s63, 0x1a000
	s_mov_b32 s77, 0xc000
	s_mov_b32 s76, 0xe000
	s_movk_i32 s75, 0x3400
	v_readlane_b32 s74, v255, 38

.LBB0_114:
	v_or_b32_e32 v2, s4, v14
	s_or_b32 s5, s4, 2
	s_or_b32 s8, s4, 4
	v_lshl_add_u64 v[16:17], v[2:3], 2, s[38:39]
	v_mad_u32_u24 v30, v2, s67, v15
	v_or_b32_e32 v29, s5, v14
	v_add_u32_e32 v2, s4, v14
	s_or_b32 s9, s4, 6
	v_or_b32_e32 v34, s8, v14
	global_load_dword v48, v[16:17], off nt
	v_lshl_add_u64 v[16:17], v[2:3], 2, s[38:39]
	v_mad_u32_u24 v2, v29, s67, v15
	s_or_b32 s16, s4, 8
	v_or_b32_e32 v35, s9, v14
	v_ashrrev_i32_e32 v31, 31, v30
	v_lshl_add_u64 v[32:33], v[2:3], 2, s[36:37]
	v_mad_u32_u24 v2, v34, s67, v15
	s_or_b32 s17, s4, 10
	v_or_b32_e32 v36, s16, v14
	v_lshl_add_u64 v[30:31], v[30:31], 2, s[36:37]
	global_load_dword v29, v[16:17], off offset:8 nt
	global_load_dword v34, v[16:17], off offset:16 nt
	global_load_dword v49, v[16:17], off offset:24 nt
	global_load_dword v52, v[16:17], off offset:32 nt
	global_load_dword v53, v[16:17], off offset:40 nt
	global_load_dword v54, v[16:17], off offset:48 nt
	global_load_dword v55, v[16:17], off offset:56 nt
	global_load_dword v56, v[16:17], off offset:64 nt
	global_load_dword v57, v[16:17], off offset:72 nt
	global_load_dword v58, v[16:17], off offset:80 nt
	global_load_dword v59, v[16:17], off offset:88 nt
	global_load_dword v60, v[16:17], off offset:96 nt
	global_load_dword v61, v[16:17], off offset:104 nt
	global_load_dword v62, v[16:17], off offset:112 nt
	global_load_dword v63, v[16:17], off offset:120 nt
	global_load_dword v64, v[30:31], off nt
	v_lshl_add_u64 v[16:17], v[2:3], 2, s[36:37]
	v_mad_u32_u24 v2, v35, s67, v15
	s_or_b32 s56, s4, 12
	v_or_b32_e32 v37, s17, v14
	global_load_dword v32, v[32:33], off nt
	s_nop 0
	global_load_dword v33, v[16:17], off nt
	v_lshl_add_u64 v[16:17], v[2:3], 2, s[36:37]
	v_mad_u32_u24 v2, v36, s67, v15
	s_or_b32 s59, s4, 14
	v_or_b32_e32 v38, s56, v14
	v_lshl_add_u64 v[30:31], v[2:3], 2, s[36:37]
	v_mad_u32_u24 v2, v37, s67, v15
	s_or_b32 s62, s4, 16
	v_or_b32_e32 v39, s59, v14
	global_load_dword v35, v[16:17], off nt
	global_load_dword v36, v[30:31], off nt
	v_lshl_add_u64 v[16:17], v[2:3], 2, s[36:37]
	v_mad_u32_u24 v2, v38, s67, v15
	s_or_b32 s63, s4, 18
	v_or_b32_e32 v40, s62, v14
	v_lshl_add_u64 v[30:31], v[2:3], 2, s[36:37]
	v_mad_u32_u24 v2, v39, s67, v15
	s_or_b32 s68, s4, 20
	v_or_b32_e32 v41, s63, v14
	global_load_dword v37, v[16:17], off nt
	global_load_dword v38, v[30:31], off nt
	v_lshl_add_u64 v[16:17], v[2:3], 2, s[36:37]
	v_mad_u32_u24 v2, v40, s67, v15
	s_or_b32 s69, s4, 22
	v_or_b32_e32 v42, s68, v14
	v_lshl_add_u64 v[30:31], v[2:3], 2, s[36:37]
	v_mad_u32_u24 v2, v41, s67, v15
	s_or_b32 s74, s4, 24
	v_or_b32_e32 v43, s69, v14
	global_load_dword v39, v[16:17], off nt
	global_load_dword v40, v[30:31], off nt
	v_lshl_add_u64 v[16:17], v[2:3], 2, s[36:37]
	v_mad_u32_u24 v2, v42, s67, v15
	s_or_b32 s75, s4, 26
	v_or_b32_e32 v44, s74, v14
	global_load_dword v41, v[16:17], off nt
	v_lshl_add_u64 v[16:17], v[2:3], 2, s[36:37]
	v_mad_u32_u24 v2, v43, s67, v15
	s_or_b32 s76, s4, 28
	v_or_b32_e32 v45, s75, v14
	v_lshl_add_u64 v[30:31], v[2:3], 2, s[36:37]
	v_mad_u32_u24 v2, v44, s67, v15
	s_or_b32 s77, s4, 30
	v_or_b32_e32 v46, s76, v14
	global_load_dword v42, v[16:17], off nt
	global_load_dword v43, v[30:31], off nt
	v_lshl_add_u64 v[16:17], v[2:3], 2, s[36:37]
	v_mad_u32_u24 v2, v45, s67, v15
	v_or_b32_e32 v47, s77, v14
	v_lshl_add_u64 v[30:31], v[2:3], 2, s[36:37]
	v_mad_u32_u24 v2, v46, s67, v15
	global_load_dword v44, v[16:17], off nt
	s_nop 0
	global_load_dword v30, v[30:31], off nt
	v_lshl_add_u64 v[16:17], v[2:3], 2, s[36:37]
	v_mad_u32_u24 v2, v47, s67, v15
	global_load_dword v31, v[16:17], off nt
	v_lshl_add_u64 v[16:17], v[2:3], 2, s[36:37]
	global_load_dword v2, v[16:17], off nt
	v_or_b32_e32 v16, s4, v18
	v_or_b32_e32 v17, s5, v18
	v_mad_u32_u24 v16, v16, s66, v19
	v_or_b32_e32 v45, s8, v18
	v_or_b32_e32 v46, s9, v18
	v_or_b32_e32 v47, s16, v18
	v_mad_u32_u24 v17, v17, s66, v19
	v_or_b32_e32 v65, s17, v18
	v_or_b32_e32 v66, s56, v18
	v_mad_u32_u24 v45, v45, s66, v19
	v_mad_u32_u24 v46, v46, s66, v19
	v_mad_u32_u24 v47, v47, s66, v19
	v_or_b32_e32 v67, s59, v18
	v_or_b32_e32 v68, s62, v18
	v_mad_u32_u24 v65, v65, s66, v19
	v_mad_u32_u24 v66, v66, s66, v19
	v_or_b32_e32 v69, s63, v18
	v_or_b32_e32 v70, s68, v18
	v_mad_u32_u24 v67, v67, s66, v19
	v_mad_u32_u24 v68, v68, s66, v19
	v_or_b32_e32 v71, s69, v18
	v_or_b32_e32 v72, s74, v18
	s_waitcnt vmcnt(0)
	v_mul_f32_e32 v48, v48, v64
	v_mad_u32_u24 v69, v69, s66, v19
	v_mad_u32_u24 v70, v70, s66, v19
	v_or_b32_e32 v73, s75, v18
	s_waitcnt vmcnt(14)
	v_mul_f32_e32 v29, v29, v32
	s_waitcnt vmcnt(13)
	v_mul_f32_e32 v32, v34, v33
	ds_write_b32 v16, v48
	ds_write_b32 v17, v29
	ds_write_b32 v45, v32
	v_or_b32_e32 v74, s76, v18
	v_mad_u32_u24 v71, v71, s66, v19
	v_mad_u32_u24 v72, v72, s66, v19
	s_and_b64 vcc, exec, s[40:41]
	s_mov_b64 s[40:41], 0
	s_waitcnt vmcnt(12)
	v_mul_f32_e32 v16, v49, v35
	s_waitcnt vmcnt(11)
	v_mul_f32_e32 v17, v52, v36
	ds_write_b32 v46, v16
	ds_write_b32 v47, v17
	v_or_b32_e32 v75, s77, v18
	s_mov_b32 s4, 32
	v_mad_u32_u24 v73, v73, s66, v19
	v_mad_u32_u24 v74, v74, s66, v19
	v_mad_u32_u24 v75, v75, s66, v19
	s_waitcnt vmcnt(10)
	v_mul_f32_e32 v16, v53, v37
	s_waitcnt vmcnt(9)
	v_mul_f32_e32 v17, v54, v38
	ds_write_b32 v65, v16
	ds_write_b32 v66, v17
	s_waitcnt vmcnt(8)
	v_mul_f32_e32 v16, v55, v39
	s_waitcnt vmcnt(7)
	v_mul_f32_e32 v17, v56, v40
	ds_write_b32 v67, v16
	ds_write_b32 v68, v17
	s_waitcnt vmcnt(6)
	v_mul_f32_e32 v16, v57, v41
	ds_write_b32 v69, v16
	s_waitcnt vmcnt(5)
	v_mul_f32_e32 v17, v58, v42
	s_waitcnt vmcnt(4)
	v_mul_f32_e32 v16, v59, v43
	ds_write_b32 v70, v17
	ds_write_b32 v71, v16
	s_waitcnt vmcnt(3)
	v_mul_f32_e32 v17, v60, v44
	s_waitcnt vmcnt(2)
	v_mul_f32_e32 v16, v61, v30
	ds_write_b32 v72, v17
	ds_write_b32 v73, v16
	s_waitcnt vmcnt(1)
	v_mul_f32_e32 v17, v62, v31
	s_waitcnt vmcnt(0)
	v_mul_f32_e32 v2, v63, v2
	ds_write_b32 v74, v17
	ds_write_b32 v75, v2
	s_cbranch_vccnz .LBB0_114
	s_waitcnt lgkmcnt(0)
	ds_read2_b32 v[30:31], v21 offset1:8
	ds_read2_b32 v[34:35], v21 offset0:33 offset1:41
	ds_read2_b32 v[36:37], v21 offset0:66 offset1:74
	ds_read2_b32 v[38:39], v21 offset0:99 offset1:107
	ds_read2_b32 v[40:41], v21 offset0:132 offset1:140
	ds_read2_b32 v[42:43], v21 offset0:165 offset1:173
	s_waitcnt lgkmcnt(5)
	v_bfe_u32 v2, v30, 16, 1
	v_add3_u32 v2, v30, v2, s1
	s_waitcnt lgkmcnt(4)
	v_bfe_u32 v14, v34, 16, 1
	v_lshrrev_b32_e32 v2, 16, v2
	v_add3_u32 v14, v34, v14, s1
	v_and_or_b32 v14, v14, s0, v2
	s_waitcnt lgkmcnt(3)
	v_bfe_u32 v2, v36, 16, 1
	v_add3_u32 v2, v36, v2, s1
	s_waitcnt lgkmcnt(2)
	v_bfe_u32 v15, v38, 16, 1
	ds_read2_b32 v[44:45], v21 offset0:198 offset1:206
	v_lshrrev_b32_e32 v2, 16, v2
	v_add3_u32 v15, v38, v15, s1
	ds_read2_b32 v[46:47], v21 offset0:231 offset1:239
	v_and_or_b32 v15, v15, s0, v2
	s_waitcnt lgkmcnt(3)
	v_bfe_u32 v2, v40, 16, 1
	v_add3_u32 v2, v40, v2, s1
	s_waitcnt lgkmcnt(2)
	v_bfe_u32 v16, v42, 16, 1
	v_lshrrev_b32_e32 v2, 16, v2
	v_add3_u32 v16, v42, v16, s1
	v_and_or_b32 v16, v16, s0, v2
	s_waitcnt lgkmcnt(1)
	v_bfe_u32 v2, v44, 16, 1
	v_add3_u32 v2, v44, v2, s1
	s_waitcnt lgkmcnt(0)
	v_bfe_u32 v17, v46, 16, 1
	v_lshrrev_b32_e32 v2, 16, v2
	v_add3_u32 v17, v46, v17, s1
	s_lshl_b32 s56, s7, 1
	v_and_or_b32 v17, v17, s0, v2
	v_or_b32_e32 v2, s6, v20
	v_lshl_add_u64 v[32:33], v[8:9], 0, s[56:57]
	v_lshlrev_b32_e32 v2, 10, v2
	v_lshl_add_u64 v[48:49], v[32:33], 0, v[2:3]
	v_bfe_u32 v2, v31, 16, 1
	global_store_dwordx4 v[48:49], v[14:17], off
	v_add3_u32 v2, v31, v2, s1
	v_lshrrev_b32_e32 v2, 16, v2
	v_bfe_u32 v14, v35, 16, 1
	v_add3_u32 v14, v35, v14, s1
	v_and_or_b32 v14, v14, s0, v2
	v_bfe_u32 v2, v37, 16, 1
	v_add3_u32 v2, v37, v2, s1
	v_bfe_u32 v15, v39, 16, 1
	v_lshrrev_b32_e32 v2, 16, v2
	v_add3_u32 v15, v39, v15, s1
	v_and_or_b32 v15, v15, s0, v2
	v_bfe_u32 v2, v41, 16, 1
	v_add3_u32 v2, v41, v2, s1
	v_bfe_u32 v16, v43, 16, 1
	v_lshrrev_b32_e32 v2, 16, v2
	v_add3_u32 v16, v43, v16, s1
	v_and_or_b32 v16, v16, s0, v2
	v_bfe_u32 v2, v45, 16, 1
	v_add3_u32 v2, v45, v2, s1
	v_bfe_u32 v17, v47, 16, 1
	v_lshrrev_b32_e32 v2, 16, v2
	v_add3_u32 v17, v47, v17, s1
	v_and_or_b32 v17, v17, s0, v2
	v_or_b32_e32 v2, s6, v22
	v_lshlrev_b32_e32 v2, 10, v2
	ds_read2_b32 v[30:31], v21 offset0:16 offset1:24
	v_lshl_add_u64 v[34:35], v[32:33], 0, v[2:3]
	global_store_dwordx4 v[34:35], v[14:17], off
	ds_read2_b32 v[34:35], v21 offset0:49 offset1:57
	ds_read2_b32 v[36:37], v21 offset0:82 offset1:90
	ds_read2_b32 v[38:39], v21 offset0:115 offset1:123
	s_waitcnt lgkmcnt(3)
	v_bfe_u32 v2, v30, 16, 1
	v_add3_u32 v2, v30, v2, s1
	s_waitcnt lgkmcnt(2)
	v_bfe_u32 v14, v34, 16, 1
	ds_read2_b32 v[40:41], v21 offset0:148 offset1:156
	v_lshrrev_b32_e32 v2, 16, v2
	v_add3_u32 v14, v34, v14, s1
	ds_read2_b32 v[42:43], v21 offset0:181 offset1:189
	v_and_or_b32 v14, v14, s0, v2
	s_waitcnt lgkmcnt(3)
	v_bfe_u32 v2, v36, 16, 1
	v_add3_u32 v2, v36, v2, s1
	s_waitcnt lgkmcnt(2)
	v_bfe_u32 v15, v38, 16, 1
	ds_read2_b32 v[44:45], v21 offset0:214 offset1:222
	v_lshrrev_b32_e32 v2, 16, v2
	v_add3_u32 v15, v38, v15, s1
	ds_read2_b32 v[46:47], v21 offset0:247 offset1:255
	v_and_or_b32 v15, v15, s0, v2
	s_waitcnt lgkmcnt(3)
	v_bfe_u32 v2, v40, 16, 1
	v_add3_u32 v2, v40, v2, s1
	s_waitcnt lgkmcnt(2)
	v_bfe_u32 v16, v42, 16, 1
	v_lshrrev_b32_e32 v2, 16, v2
	v_add3_u32 v16, v42, v16, s1
	v_and_or_b32 v16, v16, s0, v2
	s_waitcnt lgkmcnt(1)
	v_bfe_u32 v2, v44, 16, 1
	v_add3_u32 v2, v44, v2, s1
	s_waitcnt lgkmcnt(0)
	v_bfe_u32 v17, v46, 16, 1
	v_lshrrev_b32_e32 v2, 16, v2
	v_add3_u32 v17, v46, v17, s1
	v_and_or_b32 v17, v17, s0, v2
	v_or_b32_e32 v2, s6, v23
	v_lshlrev_b32_e32 v2, 10, v2
	v_lshl_add_u64 v[48:49], v[32:33], 0, v[2:3]
	v_bfe_u32 v2, v31, 16, 1
	global_store_dwordx4 v[48:49], v[14:17], off
	v_add3_u32 v2, v31, v2, s1
	v_lshrrev_b32_e32 v2, 16, v2
	v_bfe_u32 v14, v35, 16, 1
	v_add3_u32 v14, v35, v14, s1
	v_and_or_b32 v14, v14, s0, v2
	v_bfe_u32 v2, v37, 16, 1
	v_add3_u32 v2, v37, v2, s1
	v_bfe_u32 v15, v39, 16, 1
	v_lshrrev_b32_e32 v2, 16, v2
	v_add3_u32 v15, v39, v15, s1
	v_and_or_b32 v15, v15, s0, v2
	v_bfe_u32 v2, v41, 16, 1
	v_add3_u32 v2, v41, v2, s1
	v_bfe_u32 v16, v43, 16, 1
	v_lshrrev_b32_e32 v2, 16, v2
	v_add3_u32 v16, v43, v16, s1
	v_and_or_b32 v16, v16, s0, v2
	v_bfe_u32 v2, v45, 16, 1
	v_add3_u32 v2, v45, v2, s1
	v_bfe_u32 v17, v47, 16, 1
	v_lshrrev_b32_e32 v2, 16, v2
	v_add3_u32 v17, v47, v17, s1
	v_and_or_b32 v17, v17, s0, v2
	v_or_b32_e32 v2, s6, v24
	v_lshlrev_b32_e32 v2, 10, v2
	v_lshl_add_u64 v[30:31], v[32:33], 0, v[2:3]
	global_store_dwordx4 v[30:31], v[14:17], off
	s_waitcnt lgkmcnt(0)
	s_mov_b32 s62, 0x18000
	s_mov_b32 s63, 0x1a000
	s_mov_b32 s77, 0xc000
	s_mov_b32 s76, 0xe000
	s_movk_i32 s75, 0x3400
	v_readlane_b32 s74, v255, 38

.LBB0_118:
	v_or_b32_e32 v30, s62, v14
	s_or_b32 s5, s62, 2
	s_ashr_i32 s63, s62, 31
	s_or_b32 s6, s62, 4
	s_or_b32 s7, s62, 6
	s_or_b32 s8, s62, 8
	s_or_b32 s9, s62, 10
	s_or_b32 s37, s62, 12
	s_or_b32 s56, s62, 14
	s_or_b32 s59, s62, 16
	s_or_b32 s68, s62, 18
	s_or_b32 s69, s62, 20
	s_or_b32 s76, s62, 22
	s_or_b32 s77, s62, 24
	s_or_b32 s78, s62, 26
	s_or_b32 s79, s62, 28
	s_or_b32 s80, s62, 30
	v_ashrrev_i32_e32 v31, 31, v30
	v_mad_i64_i32 v[32:33], s[16:17], v30, s26, v[16:17]
	v_or_b32_e32 v29, s5, v14
	v_lshl_add_u64 v[34:35], s[62:63], 0, v[14:15]
	v_or_b32_e32 v36, s6, v14
	v_or_b32_e32 v38, s7, v14
	v_or_b32_e32 v40, s8, v14
	v_or_b32_e32 v42, s9, v14
	v_or_b32_e32 v44, s37, v14
	v_or_b32_e32 v46, s56, v14
	v_or_b32_e32 v48, s59, v14
	v_or_b32_e32 v52, s68, v14
	v_or_b32_e32 v54, s69, v14
	v_or_b32_e32 v56, s76, v14
	v_or_b32_e32 v58, s77, v14
	v_or_b32_e32 v60, s78, v14
	v_or_b32_e32 v62, s79, v14
	v_or_b32_e32 v64, s80, v14
	v_lshl_add_u64 v[30:31], v[30:31], 2, s[74:75]
	global_load_dword v66, v[32:33], off nt
	v_lshl_add_u64 v[32:33], v[34:35], 2, s[74:75]
	v_mad_i64_i32 v[34:35], s[16:17], v29, s26, v[16:17]
	v_mad_i64_i32 v[36:37], s[16:17], v36, s26, v[16:17]
	v_mad_i64_i32 v[38:39], s[16:17], v38, s26, v[16:17]
	v_mad_i64_i32 v[40:41], s[16:17], v40, s26, v[16:17]
	v_mad_i64_i32 v[42:43], s[16:17], v42, s26, v[16:17]
	v_mad_i64_i32 v[44:45], s[16:17], v44, s26, v[16:17]
	v_mad_i64_i32 v[46:47], s[16:17], v46, s26, v[16:17]
	v_mad_i64_i32 v[48:49], s[16:17], v48, s26, v[16:17]
	v_mad_i64_i32 v[52:53], s[16:17], v52, s26, v[16:17]
	v_mad_i64_i32 v[54:55], s[16:17], v54, s26, v[16:17]
	v_mad_i64_i32 v[56:57], s[16:17], v56, s26, v[16:17]
	v_mad_i64_i32 v[58:59], s[16:17], v58, s26, v[16:17]
	v_mad_i64_i32 v[60:61], s[16:17], v60, s26, v[16:17]
	v_mad_i64_i32 v[62:63], s[16:17], v62, s26, v[16:17]
	v_mad_i64_i32 v[64:65], s[16:17], v64, s26, v[16:17]
	global_load_dword v29, v[30:31], off nt
	s_nop 0
	global_load_dword v30, v[32:33], off offset:8 nt
	global_load_dword v31, v[32:33], off offset:16 nt
	global_load_dword v67, v[32:33], off offset:24 nt
	global_load_dword v68, v[32:33], off offset:32 nt
	global_load_dword v69, v[32:33], off offset:40 nt
	global_load_dword v70, v[32:33], off offset:48 nt
	global_load_dword v71, v[32:33], off offset:56 nt
	global_load_dword v72, v[32:33], off offset:64 nt
	s_nop 0
	global_load_dword v34, v[34:35], off nt
	s_nop 0
	global_load_dword v35, v[36:37], off nt
	s_nop 0
	global_load_dword v36, v[38:39], off nt
	global_load_dword v37, v[40:41], off nt
	s_nop 0
	global_load_dword v38, v[42:43], off nt
	global_load_dword v39, v[44:45], off nt
	global_load_dword v40, v[46:47], off nt
	global_load_dword v41, v[48:49], off nt
	s_nop 0
	global_load_dword v42, v[32:33], off offset:72 nt
	global_load_dword v43, v[32:33], off offset:80 nt
	global_load_dword v44, v[32:33], off offset:88 nt
	global_load_dword v45, v[32:33], off offset:96 nt
	global_load_dword v46, v[32:33], off offset:104 nt
	global_load_dword v47, v[32:33], off offset:112 nt
	s_nop 0
	global_load_dword v32, v[32:33], off offset:120 nt
	s_nop 0
	global_load_dword v33, v[52:53], off nt
	global_load_dword v48, v[54:55], off nt
	global_load_dword v49, v[56:57], off nt
	s_nop 0
	global_load_dword v52, v[58:59], off nt
	global_load_dword v53, v[60:61], off nt
	global_load_dword v54, v[62:63], off nt
	global_load_dword v55, v[64:65], off nt
	v_or_b32_e32 v2, s62, v18
	s_and_b64 vcc, exec, s[40:41]
	s_mov_b64 s[40:41], 0
	v_mad_u32_u24 v2, v2, s66, v19
	v_or_b32_e32 v56, s5, v18
	v_or_b32_e32 v57, s6, v18
	v_or_b32_e32 v58, s7, v18
	v_or_b32_e32 v59, s8, v18
	v_or_b32_e32 v60, s9, v18
	v_or_b32_e32 v61, s37, v18
	v_or_b32_e32 v62, s56, v18
	v_or_b32_e32 v63, s59, v18
	v_or_b32_e32 v64, s68, v18
	v_or_b32_e32 v65, s69, v18
	v_or_b32_e32 v73, s76, v18
	v_or_b32_e32 v74, s77, v18
	v_or_b32_e32 v75, s78, v18
	v_or_b32_e32 v76, s79, v18
	v_or_b32_e32 v77, s80, v18
	s_mov_b32 s62, 32
	v_mad_u32_u24 v56, v56, s66, v19
	v_mad_u32_u24 v57, v57, s66, v19
	v_mad_u32_u24 v58, v58, s66, v19
	v_mad_u32_u24 v59, v59, s66, v19
	v_mad_u32_u24 v60, v60, s66, v19
	v_mad_u32_u24 v61, v61, s66, v19
	v_mad_u32_u24 v62, v62, s66, v19
	v_mad_u32_u24 v63, v63, s66, v19
	v_mad_u32_u24 v64, v64, s66, v19
	v_mad_u32_u24 v65, v65, s66, v19
	v_mad_u32_u24 v73, v73, s66, v19
	v_mad_u32_u24 v74, v74, s66, v19
	v_mad_u32_u24 v75, v75, s66, v19
	v_mad_u32_u24 v76, v76, s66, v19
	v_mad_u32_u24 v77, v77, s66, v19
	s_waitcnt vmcnt(0)
	v_mul_f32_e32 v29, v29, v66
	v_cndmask_b32_e64 v29, v29, 0, s[38:39]
	s_waitcnt vmcnt(21)
	v_mul_f32_e32 v30, v30, v34
	s_waitcnt vmcnt(20)
	v_mul_f32_e32 v31, v31, v35
	s_waitcnt vmcnt(19)
	v_mul_f32_e32 v34, v67, v36
	s_waitcnt vmcnt(18)
	v_mul_f32_e32 v35, v68, v37
	s_waitcnt vmcnt(17)
	v_mul_f32_e32 v36, v69, v38
	s_waitcnt vmcnt(16)
	v_mul_f32_e32 v37, v70, v39
	s_waitcnt vmcnt(15)
	v_mul_f32_e32 v38, v71, v40
	s_waitcnt vmcnt(14)
	v_mul_f32_e32 v39, v72, v41
	v_cndmask_b32_e64 v30, v30, 0, s[38:39]
	v_cndmask_b32_e64 v31, v31, 0, s[38:39]
	v_cndmask_b32_e64 v34, v34, 0, s[38:39]
	v_cndmask_b32_e64 v35, v35, 0, s[38:39]
	v_cndmask_b32_e64 v36, v36, 0, s[38:39]
	v_cndmask_b32_e64 v37, v37, 0, s[38:39]
	v_cndmask_b32_e64 v38, v38, 0, s[38:39]
	s_waitcnt vmcnt(6)
	v_mul_f32_e32 v33, v42, v33
	s_waitcnt vmcnt(5)
	v_mul_f32_e32 v40, v43, v48
	s_waitcnt vmcnt(4)
	v_mul_f32_e32 v41, v44, v49
	s_waitcnt vmcnt(3)
	v_mul_f32_e32 v42, v45, v52
	s_waitcnt vmcnt(2)
	v_mul_f32_e32 v43, v46, v53
	s_waitcnt vmcnt(1)
	v_mul_f32_e32 v44, v47, v54
	s_waitcnt vmcnt(0)
	v_mul_f32_e32 v32, v32, v55
	v_cndmask_b32_e64 v39, v39, 0, s[38:39]
	v_cndmask_b32_e64 v33, v33, 0, s[38:39]
	v_cndmask_b32_e64 v40, v40, 0, s[38:39]
	v_cndmask_b32_e64 v41, v41, 0, s[38:39]
	v_cndmask_b32_e64 v42, v42, 0, s[38:39]
	v_cndmask_b32_e64 v43, v43, 0, s[38:39]
	v_cndmask_b32_e64 v44, v44, 0, s[38:39]
	v_cndmask_b32_e64 v32, v32, 0, s[38:39]
	ds_write_b32 v2, v29
	ds_write_b32 v56, v30
	ds_write_b32 v57, v31
	ds_write_b32 v58, v34
	ds_write_b32 v59, v35
	ds_write_b32 v60, v36
	ds_write_b32 v61, v37
	ds_write_b32 v62, v38
	ds_write_b32 v63, v39
	ds_write_b32 v64, v33
	ds_write_b32 v65, v40
	ds_write_b32 v73, v41
	ds_write_b32 v74, v42
	ds_write_b32 v75, v43
	ds_write_b32 v76, v44
	ds_write_b32 v77, v32
	s_cbranch_vccnz .LBB0_118
	s_waitcnt lgkmcnt(0)
	ds_read2_b32 v[30:31], v21 offset1:8
	ds_read2_b32 v[34:35], v21 offset0:33 offset1:41
	ds_read2_b32 v[36:37], v21 offset0:66 offset1:74
	ds_read2_b32 v[38:39], v21 offset0:99 offset1:107
	ds_read2_b32 v[40:41], v21 offset0:132 offset1:140
	ds_read2_b32 v[42:43], v21 offset0:165 offset1:173
	s_waitcnt lgkmcnt(5)
	v_bfe_u32 v2, v30, 16, 1
	v_add3_u32 v2, v30, v2, s1
	s_waitcnt lgkmcnt(4)
	v_bfe_u32 v14, v34, 16, 1
	v_lshrrev_b32_e32 v2, 16, v2
	v_add3_u32 v14, v34, v14, s1
	v_and_or_b32 v14, v14, s0, v2
	s_waitcnt lgkmcnt(3)
	v_bfe_u32 v2, v36, 16, 1
	v_add3_u32 v2, v36, v2, s1
	s_waitcnt lgkmcnt(2)
	v_bfe_u32 v15, v38, 16, 1
	ds_read2_b32 v[44:45], v21 offset0:198 offset1:206
	v_lshrrev_b32_e32 v2, 16, v2
	v_add3_u32 v15, v38, v15, s1
	ds_read2_b32 v[46:47], v21 offset0:231 offset1:239
	v_and_or_b32 v15, v15, s0, v2
	s_waitcnt lgkmcnt(3)
	v_bfe_u32 v2, v40, 16, 1
	v_add3_u32 v2, v40, v2, s1
	s_waitcnt lgkmcnt(2)
	v_bfe_u32 v16, v42, 16, 1
	v_lshrrev_b32_e32 v2, 16, v2
	v_add3_u32 v16, v42, v16, s1
	v_and_or_b32 v16, v16, s0, v2
	s_waitcnt lgkmcnt(1)
	v_bfe_u32 v2, v44, 16, 1
	v_or_b32_e32 v48, s4, v20
	s_ashr_i32 s37, s36, 31
	v_add3_u32 v2, v44, v2, s1
	s_waitcnt lgkmcnt(0)
	v_bfe_u32 v17, v46, 16, 1
	v_ashrrev_i32_e32 v49, 31, v48
	v_lshl_add_u64 v[32:33], s[36:37], 1, v[10:11]
	v_lshrrev_b32_e32 v2, 16, v2
	v_add3_u32 v17, v46, v17, s1
	v_lshlrev_b64 v[48:49], 11, v[48:49]
	v_and_or_b32 v17, v17, s0, v2
	v_lshl_add_u64 v[48:49], v[32:33], 0, v[48:49]
	v_bfe_u32 v2, v31, 16, 1
	global_store_dwordx4 v[48:49], v[14:17], off
	v_add3_u32 v2, v31, v2, s1
	v_lshrrev_b32_e32 v2, 16, v2
	v_bfe_u32 v14, v35, 16, 1
	v_add3_u32 v14, v35, v14, s1
	v_and_or_b32 v14, v14, s0, v2
	v_bfe_u32 v2, v37, 16, 1
	v_add3_u32 v2, v37, v2, s1
	v_bfe_u32 v15, v39, 16, 1
	v_lshrrev_b32_e32 v2, 16, v2
	v_add3_u32 v15, v39, v15, s1
	v_and_or_b32 v15, v15, s0, v2
	v_bfe_u32 v2, v41, 16, 1
	v_add3_u32 v2, v41, v2, s1
	v_bfe_u32 v16, v43, 16, 1
	v_lshrrev_b32_e32 v2, 16, v2
	v_add3_u32 v16, v43, v16, s1
	v_and_or_b32 v16, v16, s0, v2
	v_bfe_u32 v2, v45, 16, 1
	v_or_b32_e32 v30, s4, v22
	v_add3_u32 v2, v45, v2, s1
	v_bfe_u32 v17, v47, 16, 1
	v_ashrrev_i32_e32 v31, 31, v30
	v_lshrrev_b32_e32 v2, 16, v2
	v_add3_u32 v17, v47, v17, s1
	v_lshlrev_b64 v[30:31], 11, v[30:31]
	v_and_or_b32 v17, v17, s0, v2
	ds_read2_b32 v[34:35], v21 offset0:16 offset1:24
	v_lshl_add_u64 v[30:31], v[32:33], 0, v[30:31]
	global_store_dwordx4 v[30:31], v[14:17], off
	ds_read2_b32 v[30:31], v21 offset0:49 offset1:57
	ds_read2_b32 v[36:37], v21 offset0:82 offset1:90
	ds_read2_b32 v[38:39], v21 offset0:115 offset1:123
	s_waitcnt lgkmcnt(3)
	v_bfe_u32 v2, v34, 16, 1
	v_add3_u32 v2, v34, v2, s1
	s_waitcnt lgkmcnt(2)
	v_bfe_u32 v14, v30, 16, 1
	ds_read2_b32 v[40:41], v21 offset0:148 offset1:156
	v_lshrrev_b32_e32 v2, 16, v2
	v_add3_u32 v14, v30, v14, s1
	ds_read2_b32 v[42:43], v21 offset0:181 offset1:189
	v_and_or_b32 v14, v14, s0, v2
	s_waitcnt lgkmcnt(3)
	v_bfe_u32 v2, v36, 16, 1
	v_add3_u32 v2, v36, v2, s1
	s_waitcnt lgkmcnt(2)
	v_bfe_u32 v15, v38, 16, 1
	ds_read2_b32 v[44:45], v21 offset0:214 offset1:222
	v_lshrrev_b32_e32 v2, 16, v2
	v_add3_u32 v15, v38, v15, s1
	ds_read2_b32 v[46:47], v21 offset0:247 offset1:255
	v_and_or_b32 v15, v15, s0, v2
	s_waitcnt lgkmcnt(3)
	v_bfe_u32 v2, v40, 16, 1
	v_add3_u32 v2, v40, v2, s1
	s_waitcnt lgkmcnt(2)
	v_bfe_u32 v16, v42, 16, 1
	v_lshrrev_b32_e32 v2, 16, v2
	v_add3_u32 v16, v42, v16, s1
	v_and_or_b32 v16, v16, s0, v2
	s_waitcnt lgkmcnt(1)
	v_bfe_u32 v2, v44, 16, 1
	v_or_b32_e32 v48, s4, v23
	v_add3_u32 v2, v44, v2, s1
	s_waitcnt lgkmcnt(0)
	v_bfe_u32 v17, v46, 16, 1
	v_ashrrev_i32_e32 v49, 31, v48
	v_lshrrev_b32_e32 v2, 16, v2
	v_add3_u32 v17, v46, v17, s1
	v_lshlrev_b64 v[48:49], 11, v[48:49]
	v_and_or_b32 v17, v17, s0, v2
	v_lshl_add_u64 v[48:49], v[32:33], 0, v[48:49]
	v_bfe_u32 v2, v35, 16, 1
	global_store_dwordx4 v[48:49], v[14:17], off
	v_add3_u32 v2, v35, v2, s1
	v_lshrrev_b32_e32 v2, 16, v2
	v_bfe_u32 v14, v31, 16, 1
	v_add3_u32 v14, v31, v14, s1
	v_and_or_b32 v14, v14, s0, v2
	v_bfe_u32 v2, v37, 16, 1
	v_add3_u32 v2, v37, v2, s1
	v_bfe_u32 v15, v39, 16, 1
	v_lshrrev_b32_e32 v2, 16, v2
	v_add3_u32 v15, v39, v15, s1
	v_and_or_b32 v15, v15, s0, v2
	v_bfe_u32 v2, v41, 16, 1
	v_add3_u32 v2, v41, v2, s1
	v_bfe_u32 v16, v43, 16, 1
	v_lshrrev_b32_e32 v2, 16, v2
	v_add3_u32 v16, v43, v16, s1
	v_and_or_b32 v16, v16, s0, v2
	v_bfe_u32 v2, v45, 16, 1
	v_or_b32_e32 v30, s4, v24
	v_add3_u32 v2, v45, v2, s1
	v_bfe_u32 v17, v47, 16, 1
	v_ashrrev_i32_e32 v31, 31, v30
	v_lshrrev_b32_e32 v2, 16, v2
	v_add3_u32 v17, v47, v17, s1
	v_lshlrev_b64 v[30:31], 11, v[30:31]
	v_and_or_b32 v17, v17, s0, v2
	v_lshl_add_u64 v[30:31], v[32:33], 0, v[30:31]
	global_store_dwordx4 v[30:31], v[14:17], off
	s_waitcnt lgkmcnt(0)
	s_mov_b32 s80, 0x14000
	s_mov_b32 s79, 0x16000
	s_mov_b32 s62, 0x18000
	s_mov_b32 s63, 0x1a000
	s_mov_b32 s78, 0xa000
	s_mov_b32 s77, 0xc000
	s_mov_b32 s76, 0xe000
	s_movk_i32 s75, 0x3400
	v_readlane_b32 s74, v255, 38
	s_branch .LBB0_37

.LBB0_146:
	v_bfe_u32 v6, v36, 7, 7
	v_cmp_le_u32_e32 vcc, v2, v6
	v_mov_b32_e32 v8, 0
	v_mov_b64_e32 v[6:7], v[36:37]
	s_and_saveexec_b64 s[12:13], vcc
	s_cbranch_execz .LBB0_145
	s_load_dwordx2 s[14:15], s[10:11], 0x58
	s_waitcnt lgkmcnt(0)
	v_lshl_add_u64 v[6:7], s[14:15], 0, v[4:5]
	global_load_dword v8, v[6:7], off nt
	v_ashrrev_i32_e32 v7, 31, v36
	v_mov_b32_e32 v6, v36
	s_branch .LBB0_145

.LBB0_1047:
	s_lshl_b32 s4, s64, 8
	v_mov_b32_e32 v148, v0
	s_add_i32 s4, s4, s58
	s_mov_b32 s12, 0x20000
	v_and_or_b32 v212, v148, 15, s4
	s_lshl_b32 s4, s63, 6
	s_or_b32 s4, s4, s61
	v_lshrrev_b32_e32 v2, 2, v148
	v_and_or_b32 v214, v2, 12, s4
	v_ashrrev_i32_e32 v213, 31, v212
	v_lshl_add_u64 v[246:247], v[212:213], 2, s[20:21]
	global_load_dword v232, v[246:247], off
	global_load_dword v231, v[246:247], off offset:64
	global_load_dword v230, v[246:247], off offset:128
	global_load_dword v229, v[246:247], off offset:192
	global_load_dword v228, v[246:247], off offset:512
	global_load_dword v227, v[246:247], off offset:576
	global_load_dword v226, v[246:247], off offset:640
	global_load_dword v225, v[246:247], off offset:704
	v_ashrrev_i32_e32 v140, 3, v214
	v_lshlrev_b64 v[144:145], 3, v[212:213]
	v_ashrrev_i32_e32 v141, 31, v140
	v_and_b32_e32 v147, 0x3fffff, v145
	v_and_b32_e32 v146, 0xfffffe00, v144
	v_lshl_add_u64 v[146:147], v[146:147], 0, v[140:141]
	v_lshlrev_b64 v[146:147], 10, v[146:147]
	v_lshlrev_b32_e32 v2, 1, v144
	v_lshl_add_u64 v[146:147], s[18:19], 0, v[146:147]
	v_and_b32_e32 v2, 0xf0, v2
	v_lshl_add_u64 v[144:145], v[146:147], 0, v[2:3]
	v_lshrrev_b32_e32 v2, 1, v148
	v_or_b32_e32 v194, 16, v212
	v_and_b32_e32 v2, 8, v2
	v_ashrrev_i32_e32 v195, 31, v194
	v_lshl_add_u64 v[144:145], v[144:145], 0, v[2:3]
	v_lshlrev_b64 v[154:155], 3, v[194:195]
	v_add_co_u32_e32 v146, vcc, s12, v144
	v_and_b32_e32 v157, 0x3fffff, v155
	v_and_b32_e32 v156, 0xfffffe00, v154
	v_addc_co_u32_e32 v147, vcc, 0, v145, vcc
	s_mov_b32 s5, 0x40000
	v_lshl_add_u64 v[156:157], v[156:157], 0, v[140:141]
	v_add_co_u32_e32 v148, vcc, s5, v144
	v_lshlrev_b64 v[156:157], 10, v[156:157]
	v_lshlrev_b32_e32 v154, 1, v154
	v_addc_co_u32_e32 v149, vcc, 0, v145, vcc
	s_mov_b32 s4, 0x60000
	v_lshl_add_u64 v[156:157], s[18:19], 0, v[156:157]
	v_and_b32_e32 v154, 0x3f0, v154
	v_mov_b32_e32 v155, v3
	v_add_co_u32_e32 v150, vcc, s4, v144
	v_lshl_add_u64 v[154:155], v[156:157], 0, v[154:155]
	s_nop 0
	v_addc_co_u32_e32 v151, vcc, 0, v145, vcc
	v_lshl_add_u64 v[154:155], v[154:155], 0, v[2:3]
	v_lshl_add_u64 v[152:153], v[194:195], 2, s[20:21]
	global_load_dwordx2 v[218:219], v[148:149], off nt
	global_load_dwordx2 v[216:217], v[150:151], off nt
	global_load_dwordx2 v[204:205], v[154:155], off nt
	v_add_co_u32_e32 v148, vcc, s12, v154
	v_or_b32_e32 v184, 32, v212
	s_nop 0
	v_addc_co_u32_e32 v149, vcc, 0, v155, vcc
	v_add_co_u32_e32 v150, vcc, s5, v154
	v_ashrrev_i32_e32 v185, 31, v184
	s_nop 0
	v_addc_co_u32_e32 v151, vcc, 0, v155, vcc
	v_add_co_u32_e32 v152, vcc, s4, v154
	v_or_b32_e32 v174, 48, v212
	s_nop 0
	v_addc_co_u32_e32 v153, vcc, 0, v155, vcc
	v_lshl_add_u64 v[154:155], v[184:185], 2, s[20:21]
	global_load_dwordx2 v[210:211], v[148:149], off nt
	global_load_dwordx2 v[208:209], v[150:151], off nt
	global_load_dwordx2 v[206:207], v[152:153], off nt
	v_lshlrev_b64 v[148:149], 3, v[184:185]
	v_and_b32_e32 v151, 0x3fffff, v149
	v_and_b32_e32 v150, 0xfffffe00, v148
	v_lshl_add_u64 v[150:151], v[150:151], 0, v[140:141]
	v_lshlrev_b64 v[150:151], 10, v[150:151]
	v_lshlrev_b32_e32 v148, 1, v148
	v_lshl_add_u64 v[150:151], s[18:19], 0, v[150:151]
	v_and_b32_e32 v148, 0x3f0, v148
	v_mov_b32_e32 v149, v3
	v_lshl_add_u64 v[148:149], v[150:151], 0, v[148:149]
	v_lshl_add_u64 v[148:149], v[148:149], 0, v[2:3]
	v_add_co_u32_e32 v150, vcc, s12, v148
	v_ashrrev_i32_e32 v175, 31, v174
	s_nop 0
	v_addc_co_u32_e32 v151, vcc, 0, v149, vcc
	v_add_co_u32_e32 v152, vcc, s5, v148
	v_lshl_add_u64 v[142:143], v[212:213], 2, s[20:21]
	s_nop 0
	v_addc_co_u32_e32 v153, vcc, 0, v149, vcc
	v_add_co_u32_e32 v154, vcc, s4, v148
	v_add_u32_e32 v164, 0x80, v212
	s_nop 0
	v_addc_co_u32_e32 v155, vcc, 0, v149, vcc
	global_load_dwordx2 v[192:193], v[148:149], off nt
	global_load_dwordx2 v[190:191], v[150:151], off nt
	global_load_dwordx2 v[188:189], v[152:153], off nt
	global_load_dwordx2 v[186:187], v[154:155], off nt
	v_lshlrev_b64 v[150:151], 3, v[174:175]
	v_and_b32_e32 v153, 0x3fffff, v151
	v_and_b32_e32 v152, 0xfffffe00, v150
	v_lshl_add_u64 v[152:153], v[152:153], 0, v[140:141]
	v_lshlrev_b64 v[152:153], 10, v[152:153]
	v_lshlrev_b32_e32 v150, 1, v150
	v_lshl_add_u64 v[152:153], s[18:19], 0, v[152:153]
	v_and_b32_e32 v150, 0x3f0, v150
	v_mov_b32_e32 v151, v3
	v_lshl_add_u64 v[150:151], v[152:153], 0, v[150:151]
	v_lshl_add_u64 v[150:151], v[150:151], 0, v[2:3]
	v_add_co_u32_e32 v152, vcc, s12, v150
	v_lshl_add_u64 v[148:149], v[174:175], 2, s[20:21]
	s_nop 0
	v_addc_co_u32_e32 v153, vcc, 0, v151, vcc
	v_add_co_u32_e32 v154, vcc, s5, v150
	v_ashrrev_i32_e32 v165, 31, v164
	s_nop 0
	v_addc_co_u32_e32 v155, vcc, 0, v151, vcc
	global_load_dwordx2 v[180:181], v[150:151], off nt
	global_load_dwordx2 v[178:179], v[152:153], off nt
	global_load_dwordx2 v[176:177], v[154:155], off nt
	global_load_dwordx2 v[222:223], v[144:145], off nt
	global_load_dwordx2 v[220:221], v[146:147], off nt
	v_lshlrev_b64 v[142:143], 3, v[164:165]
	v_and_b32_e32 v145, 0x3fffff, v143
	v_and_b32_e32 v144, 0xfffffe00, v142
	v_lshl_add_u64 v[144:145], v[144:145], 0, v[140:141]
	v_lshlrev_b64 v[144:145], 10, v[144:145]
	v_lshlrev_b32_e32 v142, 1, v142
	v_lshl_add_u64 v[144:145], s[18:19], 0, v[144:145]
	v_and_b32_e32 v142, 0x3f0, v142
	v_mov_b32_e32 v143, v3
	v_add_co_u32_e32 v148, vcc, s4, v150
	v_lshl_add_u64 v[142:143], v[144:145], 0, v[142:143]
	s_nop 0
	v_addc_co_u32_e32 v149, vcc, 0, v151, vcc
	v_lshl_add_u64 v[142:143], v[142:143], 0, v[2:3]
	v_add_co_u32_e32 v144, vcc, s12, v142
	v_add_u32_e32 v196, 0xb0, v212
	s_nop 0
	v_addc_co_u32_e32 v145, vcc, 0, v143, vcc
	v_add_co_u32_e32 v146, vcc, s5, v142
	v_ashrrev_i32_e32 v197, 31, v196
	s_nop 0
	v_addc_co_u32_e32 v147, vcc, 0, v143, vcc
	global_load_dwordx2 v[182:183], v[148:149], off nt
	global_load_dwordx2 v[170:171], v[142:143], off nt
	global_load_dwordx2 v[168:169], v[144:145], off nt
	global_load_dwordx2 v[166:167], v[146:147], off nt
	v_add_u32_e32 v144, 0x90, v212
	v_ashrrev_i32_e32 v145, 31, v144
	v_lshl_add_u64 v[146:147], v[144:145], 2, s[20:21]
	v_lshlrev_b64 v[144:145], 3, v[144:145]
	v_and_b32_e32 v149, 0x3fffff, v145
	v_and_b32_e32 v148, 0xfffffe00, v144
	v_lshl_add_u64 v[148:149], v[148:149], 0, v[140:141]
	v_lshlrev_b64 v[148:149], 10, v[148:149]
	v_lshlrev_b32_e32 v144, 1, v144
	v_lshl_add_u64 v[148:149], s[18:19], 0, v[148:149]
	v_and_b32_e32 v144, 0x3f0, v144
	v_mov_b32_e32 v145, v3
	v_add_co_u32_e32 v142, vcc, s4, v142
	v_lshl_add_u64 v[144:145], v[148:149], 0, v[144:145]
	s_nop 0
	v_addc_co_u32_e32 v143, vcc, 0, v143, vcc
	v_lshl_add_u64 v[144:145], v[144:145], 0, v[2:3]
	v_add_co_u32_e32 v148, vcc, s12, v144
	v_lshl_add_u64 v[198:199], v[196:197], 2, s[20:21]
	s_nop 0
	v_addc_co_u32_e32 v149, vcc, 0, v145, vcc
	global_load_dwordx2 v[172:173], v[142:143], off nt
	global_load_dwordx2 v[158:159], v[144:145], off nt
	global_load_dwordx2 v[156:157], v[148:149], off nt
	v_add_u32_e32 v146, 0xa0, v212
	v_ashrrev_i32_e32 v147, 31, v146
	v_lshl_add_u64 v[148:149], v[146:147], 2, s[20:21]
	v_lshlrev_b64 v[146:147], 3, v[146:147]
	v_and_b32_e32 v151, 0x3fffff, v147
	v_and_b32_e32 v150, 0xfffffe00, v146
	v_lshl_add_u64 v[150:151], v[150:151], 0, v[140:141]
	v_add_co_u32_e32 v142, vcc, s5, v144
	v_lshlrev_b64 v[150:151], 10, v[150:151]
	v_lshlrev_b32_e32 v146, 1, v146
	v_addc_co_u32_e32 v143, vcc, 0, v145, vcc
	v_lshl_add_u64 v[150:151], s[18:19], 0, v[150:151]
	v_and_b32_e32 v146, 0x3f0, v146
	v_mov_b32_e32 v147, v3
	v_add_co_u32_e32 v144, vcc, s4, v144
	v_lshl_add_u64 v[146:147], v[150:151], 0, v[146:147]
	s_nop 0
	v_addc_co_u32_e32 v145, vcc, 0, v145, vcc
	v_lshl_add_u64 v[146:147], v[146:147], 0, v[2:3]
	global_load_dwordx2 v[162:163], v[142:143], off nt
	global_load_dwordx2 v[160:161], v[144:145], off nt
	s_nop 0
	global_load_dwordx2 v[148:149], v[146:147], off nt
	v_add_co_u32_e32 v142, vcc, s12, v146
	s_waitcnt vmcnt(25)
	v_mul_f32_e32 v225, 0xbfb8aa3b, v225
	v_mul_f32_e32 v226, 0xbfb8aa3b, v226
	v_mul_f32_e32 v227, 0xbfb8aa3b, v227
	v_mul_f32_e32 v228, 0xbfb8aa3b, v228
	v_mul_f32_e32 v229, 0xbfb8aa3b, v229
	v_mul_f32_e32 v230, 0xbfb8aa3b, v230
	v_mul_f32_e32 v231, 0xbfb8aa3b, v231
	v_mul_f32_e32 v232, 0xbfb8aa3b, v232
	v_mul_f32_e32 v108, v231, v108
	v_addc_co_u32_e32 v143, vcc, 0, v147, vcc
	v_add_co_u32_e32 v144, vcc, s5, v146
	v_mul_f32_e32 v124, v232, v124
	s_nop 0
	v_addc_co_u32_e32 v145, vcc, 0, v147, vcc
	v_add_co_u32_e32 v146, vcc, s4, v146
	s_nop 0
	v_addc_co_u32_e32 v147, vcc, 0, v147, vcc
	global_load_dwordx2 v[154:155], v[142:143], off nt
	global_load_dwordx2 v[152:153], v[144:145], off nt
	global_load_dwordx2 v[150:151], v[146:147], off nt
	v_lshlrev_b64 v[142:143], 3, v[196:197]
	v_and_b32_e32 v145, 0x3fffff, v143
	v_and_b32_e32 v144, 0xfffffe00, v142
	v_lshl_add_u64 v[140:141], v[144:145], 0, v[140:141]
	v_lshlrev_b64 v[140:141], 10, v[140:141]
	v_lshlrev_b32_e32 v142, 1, v142
	v_lshl_add_u64 v[140:141], s[18:19], 0, v[140:141]
	v_and_b32_e32 v142, 0x3f0, v142
	v_mov_b32_e32 v143, v3
	v_lshl_add_u64 v[140:141], v[140:141], 0, v[142:143]
	v_lshl_add_u64 v[140:141], v[140:141], 0, v[2:3]
	v_mul_f32_e32 v2, v232, v128
	v_mul_f32_e32 v128, v232, v129
	v_exp_f32_e32 v2, v2
	v_exp_f32_e32 v129, v128
	v_mul_f32_e32 v125, v232, v125
	v_add_f32_e32 v2, 1.0, v2
	v_rcp_f32_e32 v128, v2
	v_add_f32_e32 v2, 1.0, v129
	v_mul_f32_e32 v129, v232, v130
	v_exp_f32_e32 v130, v129
	v_mul_f32_e32 v129, v232, v131
	v_exp_f32_e32 v131, v129
	v_exp_f32_e32 v124, v124
	v_exp_f32_e32 v125, v125
	v_rcp_f32_e32 v129, v2
	v_add_f32_e32 v2, 1.0, v130
	v_rcp_f32_e32 v130, v2
	v_add_f32_e32 v2, 1.0, v131
	v_rcp_f32_e32 v131, v2
	v_add_f32_e32 v2, 1.0, v124
	v_rcp_f32_e32 v124, v2
	v_add_f32_e32 v2, 1.0, v125
	v_mul_f32_e32 v125, v232, v126
	v_exp_f32_e32 v126, v125
	v_mul_f32_e32 v125, v232, v127
	v_mul_f32_e32 v120, v232, v120
	v_exp_f32_e32 v127, v125
	v_mul_f32_e32 v121, v232, v121
	v_exp_f32_e32 v120, v120
	v_exp_f32_e32 v121, v121
	v_rcp_f32_e32 v125, v2
	v_add_f32_e32 v2, 1.0, v126
	v_rcp_f32_e32 v126, v2
	v_add_f32_e32 v2, 1.0, v127
	v_rcp_f32_e32 v127, v2
	v_add_f32_e32 v2, 1.0, v120
	v_rcp_f32_e32 v120, v2
	v_add_f32_e32 v2, 1.0, v121
	v_mul_f32_e32 v121, v232, v122
	v_exp_f32_e32 v122, v121
	v_mul_f32_e32 v121, v232, v123
	v_mul_f32_e32 v116, v232, v116
	v_exp_f32_e32 v123, v121
	v_mul_f32_e32 v117, v232, v117
	v_exp_f32_e32 v116, v116
	v_exp_f32_e32 v117, v117
	v_rcp_f32_e32 v121, v2
	v_add_f32_e32 v2, 1.0, v122
	v_rcp_f32_e32 v122, v2
	v_add_f32_e32 v2, 1.0, v123
	v_rcp_f32_e32 v123, v2
	v_add_f32_e32 v2, 1.0, v116
	v_rcp_f32_e32 v116, v2
	v_add_f32_e32 v2, 1.0, v117
	v_rcp_f32_e32 v117, v2
	v_mul_f32_e32 v2, v232, v118
	v_mul_f32_e32 v118, v232, v119
	v_exp_f32_e32 v2, v2
	v_exp_f32_e32 v119, v118
	v_add_f32_e32 v2, 1.0, v2
	v_rcp_f32_e32 v118, v2
	v_add_f32_e32 v2, 1.0, v119
	v_rcp_f32_e32 v119, v2
	v_mul_f32_e32 v2, v231, v112
	v_mul_f32_e32 v112, v231, v113
	v_exp_f32_e32 v2, v2
	v_exp_f32_e32 v113, v112
	v_mul_f32_e32 v109, v231, v109
	v_add_f32_e32 v2, 1.0, v2
	v_rcp_f32_e32 v112, v2
	v_add_f32_e32 v2, 1.0, v113
	v_mul_f32_e32 v113, v231, v114
	v_exp_f32_e32 v114, v113
	v_mul_f32_e32 v113, v231, v115
	v_exp_f32_e32 v115, v113
	v_exp_f32_e32 v108, v108
	v_exp_f32_e32 v109, v109
	v_rcp_f32_e32 v113, v2
	v_add_f32_e32 v2, 1.0, v114
	v_rcp_f32_e32 v114, v2
	v_add_f32_e32 v2, 1.0, v115
	v_rcp_f32_e32 v115, v2
	v_add_f32_e32 v2, 1.0, v108
	v_rcp_f32_e32 v108, v2
	v_add_f32_e32 v2, 1.0, v109
	v_mul_f32_e32 v109, v231, v110
	v_exp_f32_e32 v110, v109
	v_mul_f32_e32 v109, v231, v111
	v_mul_f32_e32 v104, v231, v104
	v_exp_f32_e32 v111, v109
	v_mul_f32_e32 v105, v231, v105
	v_exp_f32_e32 v104, v104
	v_exp_f32_e32 v105, v105
	v_rcp_f32_e32 v109, v2
	v_add_f32_e32 v2, 1.0, v110
	v_rcp_f32_e32 v110, v2
	v_add_f32_e32 v2, 1.0, v111
	v_rcp_f32_e32 v111, v2
	v_add_f32_e32 v2, 1.0, v104
	v_rcp_f32_e32 v104, v2
	v_add_f32_e32 v2, 1.0, v105
	v_mul_f32_e32 v105, v231, v106
	v_exp_f32_e32 v106, v105
	v_mul_f32_e32 v105, v231, v107
	v_mul_f32_e32 v100, v231, v100
	v_exp_f32_e32 v107, v105
	v_mul_f32_e32 v101, v231, v101
	v_exp_f32_e32 v100, v100
	v_exp_f32_e32 v101, v101
	v_rcp_f32_e32 v105, v2
	v_add_f32_e32 v2, 1.0, v106
	v_rcp_f32_e32 v106, v2
	v_add_f32_e32 v2, 1.0, v107
	v_rcp_f32_e32 v107, v2
	v_add_f32_e32 v2, 1.0, v100
	v_rcp_f32_e32 v100, v2
	v_add_f32_e32 v2, 1.0, v101
	v_rcp_f32_e32 v101, v2
	v_mul_f32_e32 v2, v231, v102
	v_mul_f32_e32 v102, v231, v103
	v_exp_f32_e32 v2, v2
	v_exp_f32_e32 v103, v102
	v_mul_f32_e32 v92, v230, v92
	v_add_f32_e32 v2, 1.0, v2
	v_rcp_f32_e32 v102, v2
	v_add_f32_e32 v2, 1.0, v103
	v_rcp_f32_e32 v103, v2
	v_mul_f32_e32 v2, v230, v96
	v_mul_f32_e32 v96, v230, v97
	v_exp_f32_e32 v2, v2
	v_exp_f32_e32 v97, v96
	v_add_f32_e32 v2, 1.0, v2
	v_rcp_f32_e32 v96, v2
	v_add_f32_e32 v2, 1.0, v97
	v_mul_f32_e32 v97, v230, v98
	v_exp_f32_e32 v98, v97
	v_mul_f32_e32 v97, v230, v99
	v_exp_f32_e32 v99, v97
	v_mul_f32_e32 v93, v230, v93
	v_exp_f32_e32 v92, v92
	v_exp_f32_e32 v93, v93
	v_rcp_f32_e32 v97, v2
	v_add_f32_e32 v2, 1.0, v98
	v_rcp_f32_e32 v98, v2
	v_add_f32_e32 v2, 1.0, v99
	v_rcp_f32_e32 v99, v2
	v_add_f32_e32 v2, 1.0, v92
	v_rcp_f32_e32 v92, v2
	v_add_f32_e32 v2, 1.0, v93
	v_mul_f32_e32 v93, v230, v94
	v_exp_f32_e32 v94, v93
	v_mul_f32_e32 v93, v230, v95
	v_mul_f32_e32 v88, v230, v88
	v_exp_f32_e32 v95, v93
	v_mul_f32_e32 v89, v230, v89
	v_exp_f32_e32 v88, v88
	v_exp_f32_e32 v89, v89
	v_rcp_f32_e32 v93, v2
	v_add_f32_e32 v2, 1.0, v94
	v_rcp_f32_e32 v94, v2
	v_add_f32_e32 v2, 1.0, v95
	v_rcp_f32_e32 v95, v2
	v_add_f32_e32 v2, 1.0, v88
	v_rcp_f32_e32 v88, v2
	v_add_f32_e32 v2, 1.0, v89
	v_mul_f32_e32 v89, v230, v90
	v_exp_f32_e32 v90, v89
	v_mul_f32_e32 v89, v230, v91
	v_mul_f32_e32 v84, v230, v84
	v_exp_f32_e32 v91, v89
	v_mul_f32_e32 v85, v230, v85
	v_exp_f32_e32 v84, v84
	v_exp_f32_e32 v85, v85
	v_rcp_f32_e32 v89, v2
	v_add_f32_e32 v2, 1.0, v90
	v_rcp_f32_e32 v90, v2
	v_add_f32_e32 v2, 1.0, v91
	v_rcp_f32_e32 v91, v2
	v_add_f32_e32 v2, 1.0, v84
	v_rcp_f32_e32 v84, v2
	v_add_f32_e32 v2, 1.0, v85
	v_rcp_f32_e32 v85, v2
	v_mul_f32_e32 v2, v230, v86
	v_mul_f32_e32 v86, v230, v87
	v_exp_f32_e32 v2, v2
	v_exp_f32_e32 v87, v86
	v_mul_f32_e32 v76, v229, v76
	v_add_f32_e32 v2, 1.0, v2
	v_rcp_f32_e32 v86, v2
	v_add_f32_e32 v2, 1.0, v87
	v_rcp_f32_e32 v87, v2
	v_mul_f32_e32 v2, v229, v80
	v_mul_f32_e32 v80, v229, v81
	v_exp_f32_e32 v2, v2
	v_exp_f32_e32 v81, v80
	v_add_f32_e32 v2, 1.0, v2
	v_rcp_f32_e32 v80, v2
	v_add_f32_e32 v2, 1.0, v81
	v_mul_f32_e32 v81, v229, v82
	v_exp_f32_e32 v82, v81
	v_mul_f32_e32 v81, v229, v83
	v_exp_f32_e32 v83, v81
	v_mul_f32_e32 v77, v229, v77
	v_exp_f32_e32 v76, v76
	v_exp_f32_e32 v77, v77
	v_rcp_f32_e32 v81, v2
	v_add_f32_e32 v2, 1.0, v82
	v_rcp_f32_e32 v82, v2
	v_add_f32_e32 v2, 1.0, v83
	v_rcp_f32_e32 v83, v2
	v_add_f32_e32 v2, 1.0, v76
	v_rcp_f32_e32 v76, v2
	v_add_f32_e32 v2, 1.0, v77
	v_mul_f32_e32 v77, v229, v78
	v_exp_f32_e32 v78, v77
	v_mul_f32_e32 v77, v229, v79
	v_mul_f32_e32 v72, v229, v72
	v_exp_f32_e32 v79, v77
	v_mul_f32_e32 v73, v229, v73
	v_exp_f32_e32 v72, v72
	v_exp_f32_e32 v73, v73
	v_rcp_f32_e32 v77, v2
	v_add_f32_e32 v2, 1.0, v78
	v_rcp_f32_e32 v78, v2
	v_add_f32_e32 v2, 1.0, v79
	v_rcp_f32_e32 v79, v2
	v_add_f32_e32 v2, 1.0, v72
	v_rcp_f32_e32 v72, v2
	v_add_f32_e32 v2, 1.0, v73
	v_mul_f32_e32 v73, v229, v74
	v_exp_f32_e32 v74, v73
	v_mul_f32_e32 v73, v229, v75
	v_mul_f32_e32 v68, v229, v68
	v_exp_f32_e32 v75, v73
	v_mul_f32_e32 v69, v229, v69
	v_exp_f32_e32 v68, v68
	v_exp_f32_e32 v69, v69
	v_rcp_f32_e32 v73, v2
	v_add_f32_e32 v2, 1.0, v74
	v_rcp_f32_e32 v74, v2
	v_add_f32_e32 v2, 1.0, v75
	v_rcp_f32_e32 v75, v2
	v_add_f32_e32 v2, 1.0, v68
	v_rcp_f32_e32 v68, v2
	v_add_f32_e32 v2, 1.0, v69
	v_rcp_f32_e32 v69, v2
	v_mul_f32_e32 v2, v229, v70
	v_mul_f32_e32 v70, v229, v71
	v_exp_f32_e32 v2, v2
	v_exp_f32_e32 v71, v70
	v_mul_f32_e32 v60, v228, v60
	v_add_f32_e32 v2, 1.0, v2
	v_rcp_f32_e32 v70, v2
	v_add_f32_e32 v2, 1.0, v71
	v_rcp_f32_e32 v71, v2
	v_mul_f32_e32 v2, v228, v64
	v_mul_f32_e32 v64, v228, v65
	v_exp_f32_e32 v2, v2
	v_exp_f32_e32 v65, v64
	v_add_f32_e32 v2, 1.0, v2
	v_rcp_f32_e32 v64, v2
	v_add_f32_e32 v2, 1.0, v65
	v_mul_f32_e32 v65, v228, v66
	v_exp_f32_e32 v66, v65
	v_mul_f32_e32 v65, v228, v67
	v_exp_f32_e32 v67, v65
	v_mul_f32_e32 v61, v228, v61
	v_exp_f32_e32 v60, v60
	v_exp_f32_e32 v61, v61
	v_rcp_f32_e32 v65, v2
	v_add_f32_e32 v2, 1.0, v66
	v_rcp_f32_e32 v66, v2
	v_add_f32_e32 v2, 1.0, v67
	v_rcp_f32_e32 v67, v2
	v_add_f32_e32 v2, 1.0, v60
	v_rcp_f32_e32 v60, v2
	v_add_f32_e32 v2, 1.0, v61
	v_mul_f32_e32 v61, v228, v62
	v_exp_f32_e32 v62, v61
	v_mul_f32_e32 v61, v228, v63
	v_mul_f32_e32 v56, v228, v56
	v_exp_f32_e32 v63, v61
	v_mul_f32_e32 v57, v228, v57
	v_exp_f32_e32 v56, v56
	v_exp_f32_e32 v57, v57
	v_rcp_f32_e32 v61, v2
	v_add_f32_e32 v2, 1.0, v62
	v_rcp_f32_e32 v62, v2
	v_add_f32_e32 v2, 1.0, v63
	v_rcp_f32_e32 v63, v2
	v_add_f32_e32 v2, 1.0, v56
	v_rcp_f32_e32 v56, v2
	v_add_f32_e32 v2, 1.0, v57
	v_mul_f32_e32 v57, v228, v58
	v_exp_f32_e32 v58, v57
	v_mul_f32_e32 v57, v228, v59
	v_mul_f32_e32 v52, v228, v52
	v_exp_f32_e32 v59, v57
	v_mul_f32_e32 v53, v228, v53
	v_exp_f32_e32 v52, v52
	v_exp_f32_e32 v53, v53
	v_rcp_f32_e32 v57, v2
	v_add_f32_e32 v2, 1.0, v58
	v_rcp_f32_e32 v58, v2
	v_add_f32_e32 v2, 1.0, v59
	v_rcp_f32_e32 v59, v2
	v_add_f32_e32 v2, 1.0, v52
	v_rcp_f32_e32 v52, v2
	v_add_f32_e32 v2, 1.0, v53
	v_rcp_f32_e32 v53, v2
	v_mul_f32_e32 v2, v228, v54
	v_mul_f32_e32 v54, v228, v55
	v_exp_f32_e32 v2, v2
	v_exp_f32_e32 v55, v54
	v_mul_f32_e32 v44, v227, v44
	v_add_f32_e32 v2, 1.0, v2
	v_rcp_f32_e32 v54, v2
	v_add_f32_e32 v2, 1.0, v55
	v_rcp_f32_e32 v55, v2
	v_mul_f32_e32 v2, v227, v48
	v_mul_f32_e32 v48, v227, v49
	v_exp_f32_e32 v2, v2
	v_exp_f32_e32 v49, v48
	v_add_f32_e32 v2, 1.0, v2
	v_rcp_f32_e32 v48, v2
	v_add_f32_e32 v2, 1.0, v49
	v_mul_f32_e32 v49, v227, v50
	v_exp_f32_e32 v50, v49
	v_mul_f32_e32 v49, v227, v51
	v_exp_f32_e32 v51, v49
	v_mul_f32_e32 v45, v227, v45
	v_exp_f32_e32 v44, v44
	v_exp_f32_e32 v45, v45
	v_rcp_f32_e32 v49, v2
	v_add_f32_e32 v2, 1.0, v50
	v_rcp_f32_e32 v50, v2
	v_add_f32_e32 v2, 1.0, v51
	v_rcp_f32_e32 v51, v2
	v_add_f32_e32 v2, 1.0, v44
	v_rcp_f32_e32 v44, v2
	v_add_f32_e32 v2, 1.0, v45
	v_mul_f32_e32 v45, v227, v46
	v_exp_f32_e32 v46, v45
	v_mul_f32_e32 v45, v227, v47
	v_mul_f32_e32 v40, v227, v40
	v_exp_f32_e32 v47, v45
	v_mul_f32_e32 v41, v227, v41
	v_exp_f32_e32 v40, v40
	v_exp_f32_e32 v41, v41
	v_rcp_f32_e32 v45, v2
	v_add_f32_e32 v2, 1.0, v46
	v_rcp_f32_e32 v46, v2
	v_add_f32_e32 v2, 1.0, v47
	v_rcp_f32_e32 v47, v2
	v_add_f32_e32 v2, 1.0, v40
	v_rcp_f32_e32 v40, v2
	v_add_f32_e32 v2, 1.0, v41
	v_mul_f32_e32 v41, v227, v42
	v_exp_f32_e32 v42, v41
	v_mul_f32_e32 v41, v227, v43
	v_mul_f32_e32 v36, v227, v36
	v_exp_f32_e32 v43, v41
	v_mul_f32_e32 v37, v227, v37
	v_exp_f32_e32 v36, v36
	v_exp_f32_e32 v37, v37
	v_rcp_f32_e32 v41, v2
	v_add_f32_e32 v2, 1.0, v42
	v_rcp_f32_e32 v42, v2
	v_add_f32_e32 v2, 1.0, v43
	v_rcp_f32_e32 v43, v2
	v_add_f32_e32 v2, 1.0, v36
	v_rcp_f32_e32 v36, v2
	v_add_f32_e32 v2, 1.0, v37
	v_rcp_f32_e32 v37, v2
	v_mul_f32_e32 v2, v227, v38
	v_mul_f32_e32 v38, v227, v39
	v_exp_f32_e32 v2, v2
	v_exp_f32_e32 v39, v38
	s_waitcnt vmcnt(0)
	v_add_co_u32_e32 v142, vcc, s12, v140
	v_add_f32_e32 v2, 1.0, v2
	v_rcp_f32_e32 v38, v2
	v_add_f32_e32 v2, 1.0, v39
	v_rcp_f32_e32 v39, v2
	v_mul_f32_e32 v2, v226, v32
	v_mul_f32_e32 v32, v226, v33
	v_exp_f32_e32 v2, v2
	v_addc_co_u32_e32 v143, vcc, 0, v141, vcc
	v_exp_f32_e32 v33, v32
	v_add_co_u32_e32 v196, vcc, s5, v140
	v_add_f32_e32 v2, 1.0, v2
	s_nop 0
	v_addc_co_u32_e32 v197, vcc, 0, v141, vcc
	v_add_co_u32_e32 v198, vcc, s4, v140
	v_rcp_f32_e32 v32, v2
	s_nop 0
	v_addc_co_u32_e32 v199, vcc, 0, v141, vcc
	global_load_dwordx2 v[146:147], v[140:141], off nt
	global_load_dwordx2 v[144:145], v[142:143], off nt
	s_nop 0
	global_load_dwordx2 v[142:143], v[196:197], off nt
	global_load_dwordx2 v[140:141], v[198:199], off nt
	v_lshlrev_b32_e32 v196, 16, v222
	v_and_b32_e32 v197, 0xffff0000, v222
	v_add_f32_e32 v2, 1.0, v33
	v_mul_f32_e32 v33, v226, v34
	v_pk_fma_f32 v[128:129], v[128:129], v[196:197], 0 op_sel_hi:[1,1,0]
	v_lshlrev_b32_e32 v196, 16, v220
	v_and_b32_e32 v197, 0xffff0000, v220
	v_pk_fma_f32 v[124:125], v[124:125], v[196:197], v[128:129]
	v_lshlrev_b32_e32 v128, 16, v218
	v_and_b32_e32 v129, 0xffff0000, v218
	v_exp_f32_e32 v34, v33
	v_mul_f32_e32 v33, v226, v35
	v_pk_fma_f32 v[120:121], v[120:121], v[128:129], v[124:125]
	v_lshlrev_b32_e32 v124, 16, v216
	v_and_b32_e32 v125, 0xffff0000, v216
	v_mul_f32_e32 v28, v226, v28
	v_pk_fma_f32 v[116:117], v[116:117], v[124:125], v[120:121]
	v_lshlrev_b32_e32 v120, 16, v223
	v_and_b32_e32 v121, 0xffff0000, v223
	v_exp_f32_e32 v35, v33
	v_mul_f32_e32 v29, v226, v29
	v_pk_fma_f32 v[120:121], v[130:131], v[120:121], 0 op_sel_hi:[1,1,0]
	v_lshlrev_b32_e32 v124, 16, v221
	v_and_b32_e32 v125, 0xffff0000, v221
	v_exp_f32_e32 v28, v28
	v_pk_fma_f32 v[120:121], v[126:127], v[124:125], v[120:121]
	v_lshlrev_b32_e32 v124, 16, v219
	v_and_b32_e32 v125, 0xffff0000, v219
	v_exp_f32_e32 v29, v29
	v_pk_fma_f32 v[120:121], v[122:123], v[124:125], v[120:121]
	v_lshlrev_b32_e32 v122, 16, v217
	v_and_b32_e32 v123, 0xffff0000, v217
	v_rcp_f32_e32 v33, v2
	v_add_f32_e32 v2, 1.0, v34
	v_ashrrev_i32_e32 v215, 31, v214
	v_pk_fma_f32 v[118:119], v[118:119], v[122:123], v[120:121]
	v_cvt_pk_bf16_f32 v120, v116, v117
	v_lshlrev_b64 v[116:117], 11, v[212:213]
	v_rcp_f32_e32 v34, v2
	v_add_f32_e32 v2, 1.0, v35
	v_cvt_pk_bf16_f32 v121, v118, v119
	v_lshl_add_u64 v[116:117], s[14:15], 0, v[116:117]
	v_lshlrev_b64 v[118:119], 1, v[214:215]
	v_rcp_f32_e32 v35, v2
	v_add_f32_e32 v2, 1.0, v28
	v_lshl_add_u64 v[116:117], v[116:117], 0, v[118:119]
	v_rcp_f32_e32 v28, v2
	v_add_f32_e32 v2, 1.0, v29
	v_mul_f32_e32 v29, v226, v30
	global_store_dwordx2 v[116:117], v[120:121], off
	v_lshlrev_b32_e32 v120, 16, v204
	v_and_b32_e32 v121, 0xffff0000, v204
	v_pk_fma_f32 v[112:113], v[112:113], v[120:121], 0 op_sel_hi:[1,1,0]
	v_lshlrev_b32_e32 v120, 16, v210
	v_and_b32_e32 v121, 0xffff0000, v210
	v_exp_f32_e32 v30, v29
	v_mul_f32_e32 v29, v226, v31
	v_pk_fma_f32 v[108:109], v[108:109], v[120:121], v[112:113]
	v_lshlrev_b32_e32 v112, 16, v208
	v_and_b32_e32 v113, 0xffff0000, v208
	v_mul_f32_e32 v24, v226, v24
	v_pk_fma_f32 v[104:105], v[104:105], v[112:113], v[108:109]
	v_lshlrev_b32_e32 v108, 16, v206
	v_and_b32_e32 v109, 0xffff0000, v206
	v_exp_f32_e32 v31, v29
	v_mul_f32_e32 v25, v226, v25
	v_pk_fma_f32 v[100:101], v[100:101], v[108:109], v[104:105]
	v_lshlrev_b32_e32 v104, 16, v205
	v_and_b32_e32 v105, 0xffff0000, v205
	v_exp_f32_e32 v24, v24
	v_pk_fma_f32 v[104:105], v[114:115], v[104:105], 0 op_sel_hi:[1,1,0]
	v_lshlrev_b32_e32 v108, 16, v211
	v_and_b32_e32 v109, 0xffff0000, v211
	v_exp_f32_e32 v25, v25
	v_pk_fma_f32 v[104:105], v[110:111], v[108:109], v[104:105]
	v_lshlrev_b32_e32 v108, 16, v209
	v_and_b32_e32 v109, 0xffff0000, v209
	v_rcp_f32_e32 v29, v2
	v_add_f32_e32 v2, 1.0, v30
	v_pk_fma_f32 v[104:105], v[106:107], v[108:109], v[104:105]
	v_lshlrev_b32_e32 v106, 16, v207
	v_and_b32_e32 v107, 0xffff0000, v207
	v_rcp_f32_e32 v30, v2
	v_add_f32_e32 v2, 1.0, v31
	v_pk_fma_f32 v[102:103], v[102:103], v[106:107], v[104:105]
	v_rcp_f32_e32 v31, v2
	v_add_f32_e32 v2, 1.0, v24
	v_cvt_pk_bf16_f32 v100, v100, v101
	v_cvt_pk_bf16_f32 v101, v102, v103
	v_lshlrev_b64 v[102:103], 11, v[194:195]
	v_rcp_f32_e32 v24, v2
	v_add_f32_e32 v2, 1.0, v25
	v_mul_f32_e32 v25, v226, v26
	v_lshl_add_u64 v[102:103], s[14:15], 0, v[102:103]
	v_lshl_add_u64 v[102:103], v[102:103], 0, v[118:119]
	v_exp_f32_e32 v26, v25
	v_mul_f32_e32 v25, v226, v27
	global_store_dwordx2 v[102:103], v[100:101], off
	v_lshlrev_b32_e32 v100, 16, v192
	v_and_b32_e32 v101, 0xffff0000, v192
	v_mul_f32_e32 v20, v226, v20
	v_pk_fma_f32 v[96:97], v[96:97], v[100:101], 0 op_sel_hi:[1,1,0]
	v_lshlrev_b32_e32 v100, 16, v190
	v_and_b32_e32 v101, 0xffff0000, v190
	v_exp_f32_e32 v27, v25
	v_mul_f32_e32 v21, v226, v21
	v_pk_fma_f32 v[92:93], v[92:93], v[100:101], v[96:97]
	v_lshlrev_b32_e32 v96, 16, v188
	v_and_b32_e32 v97, 0xffff0000, v188
	v_exp_f32_e32 v20, v20
	v_pk_fma_f32 v[88:89], v[88:89], v[96:97], v[92:93]
	v_lshlrev_b32_e32 v92, 16, v186
	v_and_b32_e32 v93, 0xffff0000, v186
	v_exp_f32_e32 v21, v21
	v_pk_fma_f32 v[84:85], v[84:85], v[92:93], v[88:89]
	v_lshlrev_b32_e32 v88, 16, v193
	v_and_b32_e32 v89, 0xffff0000, v193
	v_rcp_f32_e32 v25, v2
	v_add_f32_e32 v2, 1.0, v26
	v_pk_fma_f32 v[88:89], v[98:99], v[88:89], 0 op_sel_hi:[1,1,0]
	v_lshlrev_b32_e32 v92, 16, v191
	v_and_b32_e32 v93, 0xffff0000, v191
	v_rcp_f32_e32 v26, v2
	v_add_f32_e32 v2, 1.0, v27
	v_pk_fma_f32 v[88:89], v[94:95], v[92:93], v[88:89]
	v_lshlrev_b32_e32 v92, 16, v189
	v_and_b32_e32 v93, 0xffff0000, v189
	v_rcp_f32_e32 v27, v2
	v_add_f32_e32 v2, 1.0, v20
	v_pk_fma_f32 v[88:89], v[90:91], v[92:93], v[88:89]
	v_lshlrev_b32_e32 v90, 16, v187
	v_and_b32_e32 v91, 0xffff0000, v187
	v_rcp_f32_e32 v20, v2
	v_add_f32_e32 v2, 1.0, v21
	v_pk_fma_f32 v[86:87], v[86:87], v[90:91], v[88:89]
	v_rcp_f32_e32 v21, v2
	v_mul_f32_e32 v2, v226, v22
	v_cvt_pk_bf16_f32 v84, v84, v85
	v_cvt_pk_bf16_f32 v85, v86, v87
	v_lshlrev_b64 v[86:87], 11, v[184:185]
	v_mul_f32_e32 v22, v226, v23
	v_lshl_add_u64 v[86:87], s[14:15], 0, v[86:87]
	v_exp_f32_e32 v2, v2
	v_lshl_add_u64 v[86:87], v[86:87], 0, v[118:119]
	v_exp_f32_e32 v23, v22
	global_store_dwordx2 v[86:87], v[84:85], off
	v_lshlrev_b32_e32 v84, 16, v180
	v_and_b32_e32 v85, 0xffff0000, v180
	v_pk_fma_f32 v[80:81], v[80:81], v[84:85], 0 op_sel_hi:[1,1,0]
	v_lshlrev_b32_e32 v84, 16, v178
	v_and_b32_e32 v85, 0xffff0000, v178
	v_pk_fma_f32 v[76:77], v[76:77], v[84:85], v[80:81]
	v_lshlrev_b32_e32 v80, 16, v176
	v_and_b32_e32 v81, 0xffff0000, v176
	v_add_f32_e32 v2, 1.0, v2
	v_pk_fma_f32 v[72:73], v[72:73], v[80:81], v[76:77]
	v_lshlrev_b32_e32 v76, 16, v182
	v_and_b32_e32 v77, 0xffff0000, v182
	v_rcp_f32_e32 v22, v2
	v_add_f32_e32 v2, 1.0, v23
	v_pk_fma_f32 v[68:69], v[68:69], v[76:77], v[72:73]
	v_lshlrev_b32_e32 v72, 16, v181
	v_and_b32_e32 v73, 0xffff0000, v181
	v_rcp_f32_e32 v23, v2
	s_waitcnt vmcnt(7)
	v_mul_f32_e32 v2, v225, v16
	v_pk_fma_f32 v[72:73], v[82:83], v[72:73], 0 op_sel_hi:[1,1,0]
	v_lshlrev_b32_e32 v76, 16, v179
	v_and_b32_e32 v77, 0xffff0000, v179
	v_mul_f32_e32 v16, v225, v17
	v_pk_fma_f32 v[72:73], v[78:79], v[76:77], v[72:73]
	v_lshlrev_b32_e32 v76, 16, v177
	v_and_b32_e32 v77, 0xffff0000, v177
	v_exp_f32_e32 v2, v2
	v_pk_fma_f32 v[72:73], v[74:75], v[76:77], v[72:73]
	v_lshlrev_b32_e32 v74, 16, v183
	v_and_b32_e32 v75, 0xffff0000, v183
	v_exp_f32_e32 v17, v16
	v_pk_fma_f32 v[70:71], v[70:71], v[74:75], v[72:73]
	v_cvt_pk_bf16_f32 v68, v68, v69
	v_cvt_pk_bf16_f32 v69, v70, v71
	v_lshlrev_b64 v[70:71], 11, v[174:175]
	v_lshl_add_u64 v[70:71], s[14:15], 0, v[70:71]
	v_add_f32_e32 v2, 1.0, v2
	v_lshl_add_u64 v[70:71], v[70:71], 0, v[118:119]
	v_rcp_f32_e32 v16, v2
	v_add_f32_e32 v2, 1.0, v17
	v_mul_f32_e32 v17, v225, v18
	global_store_dwordx2 v[70:71], v[68:69], off
	v_lshlrev_b32_e32 v68, 16, v170
	v_and_b32_e32 v69, 0xffff0000, v170
	v_pk_fma_f32 v[64:65], v[64:65], v[68:69], 0 op_sel_hi:[1,1,0]
	v_lshlrev_b32_e32 v68, 16, v168
	v_and_b32_e32 v69, 0xffff0000, v168
	v_exp_f32_e32 v18, v17
	v_mul_f32_e32 v17, v225, v19
	v_pk_fma_f32 v[60:61], v[60:61], v[68:69], v[64:65]
	v_lshlrev_b32_e32 v64, 16, v166
	v_and_b32_e32 v65, 0xffff0000, v166
	v_mul_f32_e32 v12, v225, v12
	v_pk_fma_f32 v[56:57], v[56:57], v[64:65], v[60:61]
	v_lshlrev_b32_e32 v60, 16, v172
	v_and_b32_e32 v61, 0xffff0000, v172
	v_exp_f32_e32 v19, v17
	v_mul_f32_e32 v13, v225, v13
	v_pk_fma_f32 v[52:53], v[52:53], v[60:61], v[56:57]
	v_lshlrev_b32_e32 v56, 16, v171
	v_and_b32_e32 v57, 0xffff0000, v171
	v_exp_f32_e32 v12, v12
	v_pk_fma_f32 v[56:57], v[66:67], v[56:57], 0 op_sel_hi:[1,1,0]
	v_lshlrev_b32_e32 v60, 16, v169
	v_and_b32_e32 v61, 0xffff0000, v169
	v_exp_f32_e32 v13, v13
	v_pk_fma_f32 v[56:57], v[62:63], v[60:61], v[56:57]
	v_lshlrev_b32_e32 v60, 16, v167
	v_and_b32_e32 v61, 0xffff0000, v167
	v_rcp_f32_e32 v17, v2
	v_add_f32_e32 v2, 1.0, v18
	v_pk_fma_f32 v[56:57], v[58:59], v[60:61], v[56:57]
	v_lshlrev_b32_e32 v58, 16, v173
	v_and_b32_e32 v59, 0xffff0000, v173
	v_rcp_f32_e32 v18, v2
	v_add_f32_e32 v2, 1.0, v19
	v_pk_fma_f32 v[54:55], v[54:55], v[58:59], v[56:57]
	v_rcp_f32_e32 v19, v2
	v_add_f32_e32 v2, 1.0, v12
	v_cvt_pk_bf16_f32 v52, v52, v53
	v_cvt_pk_bf16_f32 v53, v54, v55
	v_lshlrev_b64 v[54:55], 11, v[164:165]
	v_rcp_f32_e32 v12, v2
	v_add_f32_e32 v2, 1.0, v13
	v_mul_f32_e32 v13, v225, v14
	v_lshl_add_u64 v[54:55], s[14:15], 0, v[54:55]
	v_lshl_add_u64 v[54:55], v[54:55], 0, v[118:119]
	v_exp_f32_e32 v14, v13
	v_mul_f32_e32 v13, v225, v15
	global_store_dwordx2 v[54:55], v[52:53], off
	v_lshlrev_b32_e32 v52, 16, v158
	v_and_b32_e32 v53, 0xffff0000, v158
	v_mul_f32_e32 v8, v225, v8
	v_pk_fma_f32 v[48:49], v[48:49], v[52:53], 0 op_sel_hi:[1,1,0]
	v_lshlrev_b32_e32 v52, 16, v156
	v_and_b32_e32 v53, 0xffff0000, v156
	v_exp_f32_e32 v15, v13
	v_mul_f32_e32 v9, v225, v9
	v_pk_fma_f32 v[44:45], v[44:45], v[52:53], v[48:49]
	v_lshlrev_b32_e32 v48, 16, v162
	v_and_b32_e32 v49, 0xffff0000, v162
	v_exp_f32_e32 v8, v8
	v_pk_fma_f32 v[40:41], v[40:41], v[48:49], v[44:45]
	v_lshlrev_b32_e32 v44, 16, v160
	v_and_b32_e32 v45, 0xffff0000, v160
	v_exp_f32_e32 v9, v9
	v_pk_fma_f32 v[36:37], v[36:37], v[44:45], v[40:41]
	v_lshlrev_b32_e32 v40, 16, v159
	v_and_b32_e32 v41, 0xffff0000, v159
	v_rcp_f32_e32 v13, v2
	v_add_f32_e32 v2, 1.0, v14
	v_pk_fma_f32 v[40:41], v[50:51], v[40:41], 0 op_sel_hi:[1,1,0]
	v_lshlrev_b32_e32 v44, 16, v157
	v_and_b32_e32 v45, 0xffff0000, v157
	v_rcp_f32_e32 v14, v2
	v_add_f32_e32 v2, 1.0, v15
	v_pk_fma_f32 v[40:41], v[46:47], v[44:45], v[40:41]
	v_lshlrev_b32_e32 v44, 16, v163
	v_and_b32_e32 v45, 0xffff0000, v163
	v_rcp_f32_e32 v15, v2
	v_add_f32_e32 v2, 1.0, v8
	v_pk_fma_f32 v[40:41], v[42:43], v[44:45], v[40:41]
	v_lshlrev_b32_e32 v42, 16, v161
	v_and_b32_e32 v43, 0xffff0000, v161
	v_rcp_f32_e32 v8, v2
	v_add_f32_e32 v2, 1.0, v9
	v_mul_f32_e32 v9, v225, v10
	v_pk_fma_f32 v[38:39], v[38:39], v[42:43], v[40:41]
	s_mov_b32 s4, 0x48000
	v_cvt_pk_bf16_f32 v36, v36, v37
	v_cvt_pk_bf16_f32 v37, v38, v39
	v_add_co_u32_e32 v38, vcc, s4, v116
	v_exp_f32_e32 v10, v9
	v_mul_f32_e32 v9, v225, v11
	v_addc_co_u32_e32 v39, vcc, 0, v117, vcc
	v_mul_f32_e32 v4, v225, v4
	global_store_dwordx2 v[38:39], v[36:37], off
	v_lshlrev_b32_e32 v36, 16, v148
	v_and_b32_e32 v37, 0xffff0000, v148
	v_exp_f32_e32 v11, v9
	v_mul_f32_e32 v5, v225, v5
	v_pk_fma_f32 v[32:33], v[32:33], v[36:37], 0 op_sel_hi:[1,1,0]
	v_lshlrev_b32_e32 v36, 16, v154
	v_and_b32_e32 v37, 0xffff0000, v154
	v_exp_f32_e32 v4, v4
	v_pk_fma_f32 v[28:29], v[28:29], v[36:37], v[32:33]
	v_lshlrev_b32_e32 v32, 16, v152
	v_and_b32_e32 v33, 0xffff0000, v152
	v_exp_f32_e32 v5, v5
	v_pk_fma_f32 v[24:25], v[24:25], v[32:33], v[28:29]
	v_lshlrev_b32_e32 v28, 16, v150
	v_and_b32_e32 v29, 0xffff0000, v150
	v_rcp_f32_e32 v9, v2
	v_add_f32_e32 v2, 1.0, v10
	v_pk_fma_f32 v[20:21], v[20:21], v[28:29], v[24:25]
	v_lshlrev_b32_e32 v24, 16, v149
	v_and_b32_e32 v25, 0xffff0000, v149
	v_rcp_f32_e32 v10, v2
	v_add_f32_e32 v2, 1.0, v11
	v_pk_fma_f32 v[24:25], v[34:35], v[24:25], 0 op_sel_hi:[1,1,0]
	v_lshlrev_b32_e32 v28, 16, v155
	v_and_b32_e32 v29, 0xffff0000, v155
	v_rcp_f32_e32 v11, v2
	v_add_f32_e32 v2, 1.0, v4
	v_pk_fma_f32 v[24:25], v[30:31], v[28:29], v[24:25]
	v_lshlrev_b32_e32 v28, 16, v153
	v_and_b32_e32 v29, 0xffff0000, v153
	v_rcp_f32_e32 v4, v2
	v_add_f32_e32 v2, 1.0, v5
	v_pk_fma_f32 v[24:25], v[26:27], v[28:29], v[24:25]
	v_lshlrev_b32_e32 v26, 16, v151
	v_and_b32_e32 v27, 0xffff0000, v151
	v_rcp_f32_e32 v5, v2
	v_mul_f32_e32 v2, v225, v6
	v_pk_fma_f32 v[22:23], v[22:23], v[26:27], v[24:25]
	s_mov_b32 s4, 0x50000
	v_mul_f32_e32 v6, v225, v7
	v_cvt_pk_bf16_f32 v20, v20, v21
	v_cvt_pk_bf16_f32 v21, v22, v23
	v_add_co_u32_e32 v22, vcc, s4, v116
	v_exp_f32_e32 v2, v2
	v_addc_co_u32_e32 v23, vcc, 0, v117, vcc
	v_exp_f32_e32 v7, v6
	global_store_dwordx2 v[22:23], v[20:21], off
	s_waitcnt vmcnt(10)
	v_lshlrev_b32_e32 v20, 16, v146
	v_and_b32_e32 v21, 0xffff0000, v146
	v_pk_fma_f32 v[16:17], v[16:17], v[20:21], 0 op_sel_hi:[1,1,0]
	s_waitcnt vmcnt(9)
	v_lshlrev_b32_e32 v20, 16, v144
	v_and_b32_e32 v21, 0xffff0000, v144
	v_pk_fma_f32 v[12:13], v[12:13], v[20:21], v[16:17]
	s_waitcnt vmcnt(8)
	v_lshlrev_b32_e32 v16, 16, v142
	v_and_b32_e32 v17, 0xffff0000, v142
	v_add_f32_e32 v2, 1.0, v2
	v_pk_fma_f32 v[8:9], v[8:9], v[16:17], v[12:13]
	s_waitcnt vmcnt(7)
	v_lshlrev_b32_e32 v12, 16, v140
	v_and_b32_e32 v13, 0xffff0000, v140
	v_rcp_f32_e32 v6, v2
	v_add_f32_e32 v2, 1.0, v7
	v_pk_fma_f32 v[4:5], v[4:5], v[12:13], v[8:9]
	v_rcp_f32_e32 v7, v2
	v_lshlrev_b32_e32 v8, 16, v147
	v_and_b32_e32 v9, 0xffff0000, v147
	v_pk_fma_f32 v[8:9], v[18:19], v[8:9], 0 op_sel_hi:[1,1,0]
	v_lshlrev_b32_e32 v12, 16, v145
	v_and_b32_e32 v13, 0xffff0000, v145
	v_pk_fma_f32 v[8:9], v[14:15], v[12:13], v[8:9]
	v_lshlrev_b32_e32 v12, 16, v143
	v_and_b32_e32 v13, 0xffff0000, v143
	v_pk_fma_f32 v[8:9], v[10:11], v[12:13], v[8:9]
	v_lshlrev_b32_e32 v10, 16, v141
	v_and_b32_e32 v11, 0xffff0000, v141
	v_pk_fma_f32 v[6:7], v[6:7], v[10:11], v[8:9]
	v_cvt_pk_bf16_f32 v4, v4, v5
	v_cvt_pk_bf16_f32 v5, v6, v7
	v_add_co_u32_e32 v6, vcc, 0x58000, v116
	s_mov_b64 s[4:5], -1
	s_nop 0
	v_addc_co_u32_e32 v7, vcc, 0, v117, vcc
	s_andn2_b64 vcc, exec, s[38:39]
	s_mov_b32 s77, 0xc000
	s_mov_b32 s76, 0xe000
	s_movk_i32 s75, 0x3400
	v_readlane_b32 s74, v255, 38
	global_store_dwordx2 v[6:7], v[4:5], off
	s_cbranch_vccnz .LBB0_1036
	s_andn2_b64 vcc, exec, s[10:11]
	s_cbranch_vccnz .LBB0_1035
	s_barrier
	s_branch .LBB0_1035
